# P1b stage body: straight-line swap/non-swap variants chosen by a scalar branch (no exec-masked diamonds); nt on P3 x loads and P5a conversion loads
# speedup vs baseline: 1.0332x; 1.0093x over previous
.LBB0_248:
	s_cmp_lg_u32 s26, 0
	s_cbranch_scc1 .Lp1b_XT
	s_and_b32 s5, s4, 0x10000
	v_or_b32_e32 v2, s5, v250
	v_xor_b32_e32 v6, 64, v2
	v_add_u32_e32 v68, s5, v249
	v_xor_b32_e32 v66, 64, v68
	ds_read_b128 v[26:29], v2 offset:0
	ds_read_b128 v[30:33], v6 offset:0
	ds_read_b128 v[18:21], v2 offset:2048
	ds_read_b128 v[22:25], v6 offset:2048
	ds_read_b128 v[10:13], v2 offset:4096
	ds_read_b128 v[14:17], v6 offset:4096
	ds_read_b128 v[2:5], v2 offset:6144
	ds_read_b128 v[6:9], v6 offset:6144
	ds_read_b128 v[58:61], v68 offset:0
	ds_read_b128 v[62:65], v66 offset:0
	ds_read_b128 v[42:45], v68 offset:2048
	ds_read_b128 v[46:49], v66 offset:2048
	ds_read_b128 v[50:53], v68 offset:4096
	ds_read_b128 v[54:57], v66 offset:4096
	ds_read_b128 v[34:37], v68 offset:6144
	ds_read_b128 v[38:41], v66 offset:6144
	s_waitcnt lgkmcnt(4)
	s_nop 0
	v_mfma_scale_f32_16x16x128_f8f6f4 v[194:197], v[58:65], v[26:33], v[194:197], v218, v218 op_sel_hi:[0,0,0]
	v_mfma_scale_f32_16x16x128_f8f6f4 v[190:193], v[58:65], v[18:25], v[190:193], v218, v218 op_sel_hi:[0,0,0]
	v_mfma_scale_f32_16x16x128_f8f6f4 v[186:189], v[58:65], v[10:17], v[186:189], v218, v218 op_sel_hi:[0,0,0]
	v_mfma_scale_f32_16x16x128_f8f6f4 v[182:185], v[58:65], v[2:9], v[182:185], v218, v218 op_sel_hi:[0,0,0]
	v_mfma_scale_f32_16x16x128_f8f6f4 v[178:181], v[42:49], v[26:33], v[178:181], v218, v218 op_sel_hi:[0,0,0]
	v_mfma_scale_f32_16x16x128_f8f6f4 v[174:177], v[42:49], v[18:25], v[174:177], v218, v218 op_sel_hi:[0,0,0]
	v_mfma_scale_f32_16x16x128_f8f6f4 v[170:173], v[42:49], v[10:17], v[170:173], v218, v218 op_sel_hi:[0,0,0]
	v_mfma_scale_f32_16x16x128_f8f6f4 v[166:169], v[42:49], v[2:9], v[166:169], v218, v218 op_sel_hi:[0,0,0]
	ds_read_b128 v[58:61], v68 offset:8192
	ds_read_b128 v[62:65], v66 offset:8192
	ds_read_b128 v[42:45], v68 offset:10240
	ds_read_b128 v[46:49], v66 offset:10240
	s_waitcnt lgkmcnt(4)
	v_mfma_scale_f32_16x16x128_f8f6f4 v[162:165], v[50:57], v[26:33], v[162:165], v218, v218 op_sel_hi:[0,0,0]
	v_mfma_scale_f32_16x16x128_f8f6f4 v[158:161], v[50:57], v[18:25], v[158:161], v218, v218 op_sel_hi:[0,0,0]
	v_mfma_scale_f32_16x16x128_f8f6f4 v[154:157], v[50:57], v[10:17], v[154:157], v218, v218 op_sel_hi:[0,0,0]
	v_mfma_scale_f32_16x16x128_f8f6f4 v[150:153], v[50:57], v[2:9], v[150:153], v218, v218 op_sel_hi:[0,0,0]
	v_mfma_scale_f32_16x16x128_f8f6f4 v[146:149], v[34:41], v[26:33], v[146:149], v218, v218 op_sel_hi:[0,0,0]
	v_mfma_scale_f32_16x16x128_f8f6f4 v[142:145], v[34:41], v[18:25], v[142:145], v218, v218 op_sel_hi:[0,0,0]
	v_mfma_scale_f32_16x16x128_f8f6f4 v[138:141], v[34:41], v[10:17], v[138:141], v218, v218 op_sel_hi:[0,0,0]
	v_mfma_scale_f32_16x16x128_f8f6f4 v[134:137], v[34:41], v[2:9], v[134:137], v218, v218 op_sel_hi:[0,0,0]
	ds_read_b128 v[50:53], v68 offset:12288
	ds_read_b128 v[54:57], v66 offset:12288
	ds_read_b128 v[34:37], v68 offset:14336
	ds_read_b128 v[38:41], v66 offset:14336
	s_waitcnt lgkmcnt(4)
	v_mfma_scale_f32_16x16x128_f8f6f4 v[130:133], v[58:65], v[26:33], v[130:133], v218, v218 op_sel_hi:[0,0,0]
	v_mfma_scale_f32_16x16x128_f8f6f4 v[126:129], v[58:65], v[18:25], v[126:129], v218, v218 op_sel_hi:[0,0,0]
	v_mfma_scale_f32_16x16x128_f8f6f4 v[122:125], v[58:65], v[10:17], v[122:125], v218, v218 op_sel_hi:[0,0,0]
	v_mfma_scale_f32_16x16x128_f8f6f4 v[118:121], v[58:65], v[2:9], v[118:121], v218, v218 op_sel_hi:[0,0,0]
	v_mfma_scale_f32_16x16x128_f8f6f4 v[114:117], v[42:49], v[26:33], v[114:117], v218, v218 op_sel_hi:[0,0,0]
	v_mfma_scale_f32_16x16x128_f8f6f4 v[110:113], v[42:49], v[18:25], v[110:113], v218, v218 op_sel_hi:[0,0,0]
	v_mfma_scale_f32_16x16x128_f8f6f4 v[106:109], v[42:49], v[10:17], v[106:109], v218, v218 op_sel_hi:[0,0,0]
	v_mfma_scale_f32_16x16x128_f8f6f4 v[102:105], v[42:49], v[2:9], v[102:105], v218, v218 op_sel_hi:[0,0,0]
	s_waitcnt lgkmcnt(0)
	v_mfma_scale_f32_16x16x128_f8f6f4 v[98:101], v[50:57], v[26:33], v[98:101], v218, v218 op_sel_hi:[0,0,0]
	v_mfma_scale_f32_16x16x128_f8f6f4 v[94:97], v[50:57], v[18:25], v[94:97], v218, v218 op_sel_hi:[0,0,0]
	v_mfma_scale_f32_16x16x128_f8f6f4 v[90:93], v[50:57], v[10:17], v[90:93], v218, v218 op_sel_hi:[0,0,0]
	v_mfma_scale_f32_16x16x128_f8f6f4 v[86:89], v[50:57], v[2:9], v[86:89], v218, v218 op_sel_hi:[0,0,0]
	v_mfma_scale_f32_16x16x128_f8f6f4 v[82:85], v[34:41], v[26:33], v[82:85], v218, v218 op_sel_hi:[0,0,0]
	v_mfma_scale_f32_16x16x128_f8f6f4 v[78:81], v[34:41], v[18:25], v[78:81], v218, v218 op_sel_hi:[0,0,0]
	v_mfma_scale_f32_16x16x128_f8f6f4 v[74:77], v[34:41], v[10:17], v[74:77], v218, v218 op_sel_hi:[0,0,0]
	v_mfma_scale_f32_16x16x128_f8f6f4 v[70:73], v[34:41], v[2:9], v[70:73], v218, v218 op_sel_hi:[0,0,0]
	s_branch .LBB0_225
.Lp1b_XT:
	s_and_b32 s5, s4, 0x10000
	v_or_b32_e32 v2, s5, v250
	v_xor_b32_e32 v6, 64, v2
	v_add_u32_e32 v68, s5, v249
	v_xor_b32_e32 v66, 64, v68
	ds_read_b128 v[26:29], v2 offset:0
	ds_read_b128 v[30:33], v6 offset:0
	ds_read_b128 v[18:21], v2 offset:2048
	ds_read_b128 v[22:25], v6 offset:2048
	ds_read_b128 v[10:13], v2 offset:4096
	ds_read_b128 v[14:17], v6 offset:4096
	ds_read_b128 v[2:5], v2 offset:6144
	ds_read_b128 v[6:9], v6 offset:6144
	ds_read_b128 v[58:61], v68 offset:0
	ds_read_b128 v[62:65], v66 offset:0
	ds_read_b128 v[42:45], v68 offset:2048
	ds_read_b128 v[46:49], v66 offset:2048
	ds_read_b128 v[50:53], v68 offset:4096
	ds_read_b128 v[54:57], v66 offset:4096
	ds_read_b128 v[34:37], v68 offset:6144
	ds_read_b128 v[38:41], v66 offset:6144
	s_waitcnt lgkmcnt(4)
	s_nop 0
	v_mfma_scale_f32_16x16x128_f8f6f4 v[194:197], v[26:33], v[58:65], v[194:197], v218, v218 op_sel_hi:[0,0,0]
	v_mfma_scale_f32_16x16x128_f8f6f4 v[190:193], v[18:25], v[58:65], v[190:193], v218, v218 op_sel_hi:[0,0,0]
	v_mfma_scale_f32_16x16x128_f8f6f4 v[186:189], v[10:17], v[58:65], v[186:189], v218, v218 op_sel_hi:[0,0,0]
	v_mfma_scale_f32_16x16x128_f8f6f4 v[182:185], v[2:9], v[58:65], v[182:185], v218, v218 op_sel_hi:[0,0,0]
	v_mfma_scale_f32_16x16x128_f8f6f4 v[178:181], v[26:33], v[42:49], v[178:181], v218, v218 op_sel_hi:[0,0,0]
	v_mfma_scale_f32_16x16x128_f8f6f4 v[174:177], v[18:25], v[42:49], v[174:177], v218, v218 op_sel_hi:[0,0,0]
	v_mfma_scale_f32_16x16x128_f8f6f4 v[170:173], v[10:17], v[42:49], v[170:173], v218, v218 op_sel_hi:[0,0,0]
	v_mfma_scale_f32_16x16x128_f8f6f4 v[166:169], v[2:9], v[42:49], v[166:169], v218, v218 op_sel_hi:[0,0,0]
	ds_read_b128 v[58:61], v68 offset:8192
	ds_read_b128 v[62:65], v66 offset:8192
	ds_read_b128 v[42:45], v68 offset:10240
	ds_read_b128 v[46:49], v66 offset:10240
	s_waitcnt lgkmcnt(4)
	v_mfma_scale_f32_16x16x128_f8f6f4 v[162:165], v[26:33], v[50:57], v[162:165], v218, v218 op_sel_hi:[0,0,0]
	v_mfma_scale_f32_16x16x128_f8f6f4 v[158:161], v[18:25], v[50:57], v[158:161], v218, v218 op_sel_hi:[0,0,0]
	v_mfma_scale_f32_16x16x128_f8f6f4 v[154:157], v[10:17], v[50:57], v[154:157], v218, v218 op_sel_hi:[0,0,0]
	v_mfma_scale_f32_16x16x128_f8f6f4 v[150:153], v[2:9], v[50:57], v[150:153], v218, v218 op_sel_hi:[0,0,0]
	v_mfma_scale_f32_16x16x128_f8f6f4 v[146:149], v[26:33], v[34:41], v[146:149], v218, v218 op_sel_hi:[0,0,0]
	v_mfma_scale_f32_16x16x128_f8f6f4 v[142:145], v[18:25], v[34:41], v[142:145], v218, v218 op_sel_hi:[0,0,0]
	v_mfma_scale_f32_16x16x128_f8f6f4 v[138:141], v[10:17], v[34:41], v[138:141], v218, v218 op_sel_hi:[0,0,0]
	v_mfma_scale_f32_16x16x128_f8f6f4 v[134:137], v[2:9], v[34:41], v[134:137], v218, v218 op_sel_hi:[0,0,0]
	ds_read_b128 v[50:53], v68 offset:12288
	ds_read_b128 v[54:57], v66 offset:12288
	ds_read_b128 v[34:37], v68 offset:14336
	ds_read_b128 v[38:41], v66 offset:14336
	s_waitcnt lgkmcnt(4)
	v_mfma_scale_f32_16x16x128_f8f6f4 v[130:133], v[26:33], v[58:65], v[130:133], v218, v218 op_sel_hi:[0,0,0]
	v_mfma_scale_f32_16x16x128_f8f6f4 v[126:129], v[18:25], v[58:65], v[126:129], v218, v218 op_sel_hi:[0,0,0]
	v_mfma_scale_f32_16x16x128_f8f6f4 v[122:125], v[10:17], v[58:65], v[122:125], v218, v218 op_sel_hi:[0,0,0]
	v_mfma_scale_f32_16x16x128_f8f6f4 v[118:121], v[2:9], v[58:65], v[118:121], v218, v218 op_sel_hi:[0,0,0]
	v_mfma_scale_f32_16x16x128_f8f6f4 v[114:117], v[26:33], v[42:49], v[114:117], v218, v218 op_sel_hi:[0,0,0]
	v_mfma_scale_f32_16x16x128_f8f6f4 v[110:113], v[18:25], v[42:49], v[110:113], v218, v218 op_sel_hi:[0,0,0]
	v_mfma_scale_f32_16x16x128_f8f6f4 v[106:109], v[10:17], v[42:49], v[106:109], v218, v218 op_sel_hi:[0,0,0]
	v_mfma_scale_f32_16x16x128_f8f6f4 v[102:105], v[2:9], v[42:49], v[102:105], v218, v218 op_sel_hi:[0,0,0]
	s_waitcnt lgkmcnt(0)
	v_mfma_scale_f32_16x16x128_f8f6f4 v[98:101], v[26:33], v[50:57], v[98:101], v218, v218 op_sel_hi:[0,0,0]
	v_mfma_scale_f32_16x16x128_f8f6f4 v[94:97], v[18:25], v[50:57], v[94:97], v218, v218 op_sel_hi:[0,0,0]
	v_mfma_scale_f32_16x16x128_f8f6f4 v[90:93], v[10:17], v[50:57], v[90:93], v218, v218 op_sel_hi:[0,0,0]
	v_mfma_scale_f32_16x16x128_f8f6f4 v[86:89], v[2:9], v[50:57], v[86:89], v218, v218 op_sel_hi:[0,0,0]
	v_mfma_scale_f32_16x16x128_f8f6f4 v[82:85], v[26:33], v[34:41], v[82:85], v218, v218 op_sel_hi:[0,0,0]
	v_mfma_scale_f32_16x16x128_f8f6f4 v[78:81], v[18:25], v[34:41], v[78:81], v218, v218 op_sel_hi:[0,0,0]
	v_mfma_scale_f32_16x16x128_f8f6f4 v[74:77], v[10:17], v[34:41], v[74:77], v218, v218 op_sel_hi:[0,0,0]
	v_mfma_scale_f32_16x16x128_f8f6f4 v[70:73], v[2:9], v[34:41], v[70:73], v218, v218 op_sel_hi:[0,0,0]
	s_branch .LBB0_225

; __device__ void phase3(const Params& p, unsigned char* smem) {
;     ...
;         for (int vl = lb + gs * (tid >> 8); vl < 64; vl += 2 * gs) {
;             const size_t row = (size_t)((vl >> 2) * 8 + x) * 256 + (tid & 255);
;             const float4 s0 = *(const float4*)(p.osq + row * 16), s1 = *(const float4*)(p.osq + row * 16 + 4);
;             const float4 s2 = *(const float4*)(p.osq + row * 16 + 8), s3 = *(const float4*)(p.osq + row * 16 + 12);
;             const float sa = (s0.x + s0.y + s0.z + s0.w) + (s1.x + s1.y + s1.z + s1.w);
;             const float sb = (s2.x + s2.y + s2.z + s2.w) + (s3.x + s3.y + s3.z + s3.w);
;             const float ra = 1.0f / sqrtf(sa * (1.0f / 512.0f) + EPS), rb = 1.0f / sqrtf(sb * (1.0f / 512.0f) + EPS);
;             p.rs[row] = make_float2(ra / rb, rb);
;         }
.LBB0_496:
	v_and_or_b32 v6, v3, -8, s68
	v_ashrrev_i32_e32 v7, 31, v6
	v_lshlrev_b64 v[22:23], 8, v[6:7]
	v_or_b32_e32 v22, v22, v2
	v_lshlrev_b64 v[6:7], 6, v[22:23]
	v_lshl_add_u64 v[18:19], s[70:71], 0, v[6:7]
	global_load_dwordx4 v[6:9], v[18:19], off nt
	global_load_dwordx4 v[10:13], v[18:19], off offset:16 nt
	global_load_dwordx4 v[14:17], v[18:19], off offset:32 nt
	s_nop 0
	global_load_dwordx4 v[18:21], v[18:19], off offset:48 nt
	v_add_u32_e32 v1, s3, v1
	v_cmp_lt_i32_e32 vcc, 63, v1
	s_or_b64 s[14:15], vcc, s[14:15]
	v_add_u32_e32 v3, s4, v3
	v_lshl_add_u64 v[22:23], v[22:23], 3, s[10:11]
	s_waitcnt vmcnt(3)
	v_add_f32_e32 v6, v6, v7
	s_waitcnt vmcnt(2)
	v_add_f32_e32 v7, v10, v11
	s_waitcnt vmcnt(1)
	v_add_f32_e32 v10, v14, v15
	s_waitcnt vmcnt(0)
	v_add_f32_e32 v11, v18, v19
	v_add_f32_e32 v6, v6, v8
	v_add_f32_e32 v7, v7, v12
	v_add_f32_e32 v8, v10, v16
	v_add_f32_e32 v10, v11, v20
	v_add_f32_e32 v6, v6, v9
	v_add_f32_e32 v7, v7, v13
	v_add_f32_e32 v8, v8, v17
	v_add_f32_e32 v9, v10, v21
	v_add_f32_e32 v6, v6, v7
	v_add_f32_e32 v7, v8, v9
	v_fmamk_f32 v6, v6, 0x3b000000, v4
	v_fmamk_f32 v7, v7, 0x3b000000, v4
	v_mul_f32_e32 v8, 0x4f800000, v6
	v_cmp_gt_f32_e64 s[0:1], s5, v6
	v_mul_f32_e32 v9, 0x4f800000, v7
	v_cmp_gt_f32_e32 vcc, s5, v7
	v_cndmask_b32_e64 v6, v6, v8, s[0:1]
	v_sqrt_f32_e32 v8, v6
	v_cndmask_b32_e32 v7, v7, v9, vcc
	v_sqrt_f32_e32 v9, v7
	v_add_u32_e32 v10, -1, v8
	v_add_u32_e32 v11, 1, v8
	v_add_u32_e32 v12, -1, v9
	v_fma_f32 v14, -v10, v8, v6
	v_add_u32_e32 v13, 1, v9
	v_fma_f32 v15, -v11, v8, v6
	v_fma_f32 v16, -v12, v9, v7
	v_cmp_ge_f32_e64 s[6:7], 0, v14
	v_fma_f32 v17, -v13, v9, v7
	v_cmp_lt_f32_e64 s[8:9], 0, v15
	v_cndmask_b32_e64 v8, v8, v10, s[6:7]
	v_cmp_ge_f32_e64 s[6:7], 0, v16
	v_cndmask_b32_e64 v8, v8, v11, s[8:9]
	v_mul_f32_e32 v10, 0x37800000, v8
	v_cndmask_b32_e64 v9, v9, v12, s[6:7]
	v_cmp_lt_f32_e64 s[6:7], 0, v17
	v_cndmask_b32_e64 v8, v8, v10, s[0:1]
	v_cmp_class_f32_e64 s[0:1], v6, v5
	v_cndmask_b32_e64 v9, v9, v13, s[6:7]
	v_mul_f32_e32 v11, 0x37800000, v9
	v_cndmask_b32_e32 v9, v9, v11, vcc
	v_cmp_class_f32_e32 vcc, v7, v5
	v_cndmask_b32_e64 v6, v8, v6, s[0:1]
	v_div_scale_f32 v8, s[0:1], v6, v6, 1.0
	v_cndmask_b32_e32 v7, v9, v7, vcc
	v_div_scale_f32 v10, s[0:1], v7, v7, 1.0
	v_rcp_f32_e32 v12, v8
	v_rcp_f32_e32 v13, v10
	v_div_scale_f32 v9, vcc, 1.0, v6, 1.0
	v_fma_f32 v14, -v8, v12, 1.0
	v_fma_f32 v15, -v10, v13, 1.0
	v_fmac_f32_e32 v12, v14, v12
	v_div_scale_f32 v11, s[0:1], 1.0, v7, 1.0
	v_fmac_f32_e32 v13, v15, v13
	v_mul_f32_e32 v14, v9, v12
	v_mul_f32_e32 v15, v11, v13
	v_fma_f32 v16, -v8, v14, v9
	v_fma_f32 v17, -v10, v15, v11
	v_fmac_f32_e32 v14, v16, v12
	v_fmac_f32_e32 v15, v17, v13
	v_fma_f32 v8, -v8, v14, v9
	v_fma_f32 v9, -v10, v15, v11
	v_div_fmas_f32 v8, v8, v12, v14
	s_mov_b64 vcc, s[0:1]
	v_div_fixup_f32 v6, v8, v6, 1.0
	v_div_fmas_f32 v8, v9, v13, v15
	v_div_fixup_f32 v7, v8, v7, 1.0
	v_div_scale_f32 v8, s[0:1], v7, v7, v6
	v_rcp_f32_e32 v9, v8
	v_div_scale_f32 v10, vcc, v6, v7, v6
	v_fma_f32 v11, -v8, v9, 1.0
	v_fmac_f32_e32 v9, v11, v9
	v_mul_f32_e32 v11, v10, v9
	v_fma_f32 v12, -v8, v11, v10
	v_fmac_f32_e32 v11, v12, v9
	v_fma_f32 v8, -v8, v11, v10
	v_div_fmas_f32 v8, v8, v9, v11
	v_div_fixup_f32 v6, v8, v7, v6
	global_store_dwordx2 v[22:23], v[6:7], off
	s_andn2_b64 exec, exec, s[14:15]
	s_cbranch_execnz .LBB0_496

;     __device__ __forceinline__ void epilogue(f32x4 (&acc)[8][4], const Desc& d, unsigned char* stg) const {
;         const int tid = otid(), lane = tid & 63, wid = tid >> 6, l15 = lane & 15, gq = lane >> 4;
;         const int wr = wid >> 2, wc = wid & 3;
;         const int mt = d.mt, nt = d.nt, b = mt >> 5;
;         const int c = lane & 15, rsub = lane >> 4;
;         const int col = nt * 256 + wc * 64 + c * 4;
;         float4 g1 = *(const float4*)(p.mod + b * 6144 + 2048 + col);
;         g1.x *= 1.f / (O8S * W8S); g1.y *= 1.f / (O8S * W8S); g1.z *= 1.f / (O8S * W8S); g1.w *= 1.f / (O8S * W8S);
;         const size_t rowb = (size_t)mt * 256 + wr * 128 + rsub;
;         float4 xn[4]; float fn[4];
; #pragma unroll
;         for (int i2 = 0; i2 < 4; ++i2) { xn[i2] = *(const float4*)(p.x + (rowb + i2 * 4) * D + col); fn[i2] = p.rs[rowb + i2 * 4].y; }
; #pragma unroll
;         for (int m = 0; m < 8; ++m) {
;             float4 xc[4]; float fc[4];
; #pragma unroll
;             for (int i2 = 0; i2 < 4; ++i2) { xc[i2] = xn[i2]; fc[i2] = fn[i2]; }
;             if (m < 7) {
; #pragma unroll
;                 for (int i2 = 0; i2 < 4; ++i2) { xn[i2] = *(const float4*)(p.x + (rowb + (m + 1) * 16 + i2 * 4) * D + col); fn[i2] = p.rs[rowb + (m + 1) * 16 + i2 * 4].y; }
;             }
; #pragma unroll
;             for (int n = 0; n < 4; ++n) stgf_put(stg, n, acc[m][n], l15, gq);
;             asm volatile("s_waitcnt lgkmcnt(0)" ::: "memory");
; #pragma unroll
;             for (int i2 = 0; i2 < 4; ++i2) {
;                 const int rl = i2 * 4 + rsub;
;                 const size_t row = rowb + m * 16 + i2 * 4;
;                 const f32x4 v = stgf_get(stg, rl, c);
;                 const float fsm = fc[i2];
;                 const float4 xv = xc[i2];
;                 float4 r;
;                 r.x = xv.x + g1.x * (v[0] * fsm); r.y = xv.y + g1.y * (v[1] * fsm); r.z = xv.z + g1.z * (v[2] * fsm); r.w = xv.w + g1.w * (v[3] * fsm);
;                 *(uint2*)(p.x1 + row * D + col) = pack4((f32x4){r.x, r.y, r.z, r.w});
;                 float ss = r.x * r.x + r.y * r.y + r.z * r.z + r.w * r.w;
;                 ss += __shfl_xor(ss, 8); ss += __shfl_xor(ss, 4); ss += __shfl_xor(ss, 2); ss += __shfl_xor(ss, 1);
;                 if (c == 0) p.st2[row * 16 + nt * 4 + wc] = ss;
;             }
.LBB0_533:
	s_not_b32 s0, s29
	s_lshl_b32 s0, s0, 16
	s_and_b32 s0, s0, 0x10000
	v_mov_b32_e32 v183, v0
	s_waitcnt lgkmcnt(0)
	s_barrier
	s_add_i32 s5, s3, s0
	s_lshr_b32 s0, s22, 5
	v_and_b32_e32 v205, 15, v183
	v_bfe_u32 v221, v183, 6, 2
	s_lshl_b32 s1, s4, 8
	v_lshlrev_b32_e32 v2, 6, v221
	v_lshlrev_b32_e32 v116, 2, v205
	s_mulk_i32 s0, 0x1800
	v_or3_b32 v2, v2, s1, v116
	s_ashr_i32 s1, s0, 31
	s_lshl_b64 s[0:1], s[0:1], 2
	s_add_u32 s0, s78, s0
	s_addc_u32 s1, s79, s1
	v_lshlrev_b64 v[116:117], 2, v[2:3]
	v_lshl_add_u64 v[118:119], s[0:1], 0, v[116:117]
	v_add_co_u32_e32 v118, vcc, s28, v118
	s_lshl_b64 s[0:1], s[22:23], 8
	s_nop 0
	v_addc_co_u32_e32 v119, vcc, 0, v119, vcc
	global_load_dwordx4 v[178:181], v[118:119], off nt
	v_ashrrev_i32_e32 v118, 1, v183
	v_and_b32_e32 v118, 0xffffff80, v118
	v_ashrrev_i32_e32 v119, 31, v118
	v_bfe_u32 v222, v183, 4, 2
	v_lshl_add_u64 v[176:177], s[0:1], 0, v[118:119]
	v_or_b32_e32 v176, v176, v222
	v_or_b32_e32 v200, 12, v176
	v_mov_b32_e32 v201, v177
	v_lshl_add_u64 v[118:119], v[200:201], 3, s[10:11]
	global_load_dword v204, v[118:119], off offset:4
	v_lshl_add_u64 v[118:119], v[176:177], 3, s[10:11]
	v_or_b32_e32 v210, 4, v176
	v_mov_b32_e32 v211, v177
	v_lshl_add_u64 v[184:185], s[52:53], 0, v[116:117]
	global_load_dword v182, v[118:119], off offset:4
	v_lshlrev_b64 v[118:119], 12, v[210:211]
	v_lshl_add_u64 v[118:119], v[184:185], 0, v[118:119]
	global_load_dwordx4 v[156:159], v[118:119], off nt
	v_lshl_add_u64 v[118:119], v[210:211], 3, s[10:11]
	v_or_b32_e32 v206, 8, v176
	v_mov_b32_e32 v207, v177
	global_load_dword v212, v[118:119], off offset:4
	v_lshlrev_b64 v[118:119], 12, v[206:207]
	v_lshl_add_u64 v[118:119], v[184:185], 0, v[118:119]
	v_lshlrev_b64 v[116:117], 12, v[176:177]
	global_load_dwordx4 v[148:151], v[118:119], off nt
	v_lshl_add_u64 v[118:119], v[206:207], 3, s[10:11]
	v_lshl_add_u64 v[116:117], v[184:185], 0, v[116:117]
	global_load_dword v208, v[118:119], off offset:4
	global_load_dwordx4 v[224:227], v[116:117], off nt
	v_lshlrev_b64 v[116:117], 12, v[200:201]
	v_lshl_add_u64 v[116:117], v[184:185], 0, v[116:117]
	v_or_b32_e32 v198, 16, v176
	v_mov_b32_e32 v199, v177
	global_load_dwordx4 v[152:155], v[116:117], off nt
	v_lshlrev_b64 v[116:117], 12, v[198:199]
	v_lshl_add_u64 v[116:117], v[184:185], 0, v[116:117]
	v_or_b32_e32 v186, 28, v176
	v_mov_b32_e32 v187, v177
	global_load_dwordx4 v[144:147], v[116:117], off nt
	v_lshl_add_u64 v[116:117], v[198:199], 3, s[10:11]
	v_or_b32_e32 v194, 20, v176
	v_mov_b32_e32 v195, v177
	v_lshl_add_u64 v[216:217], v[186:187], 3, s[10:11]
	global_load_dword v202, v[116:117], off offset:4
	global_load_dword v188, v[216:217], off offset:4
	v_lshlrev_b64 v[116:117], 12, v[194:195]
	v_lshl_add_u64 v[116:117], v[184:185], 0, v[116:117]
	global_load_dwordx4 v[140:143], v[116:117], off nt
	v_lshl_add_u64 v[116:117], v[194:195], 3, s[10:11]
	v_or_b32_e32 v190, 24, v176
	v_mov_b32_e32 v191, v177
	global_load_dword v196, v[116:117], off offset:4
	v_lshlrev_b64 v[116:117], 12, v[190:191]
	v_lshl_add_u64 v[116:117], v[184:185], 0, v[116:117]
	global_load_dwordx4 v[136:139], v[116:117], off nt
	v_lshl_add_u64 v[116:117], v[190:191], 3, s[10:11]
	global_load_dword v192, v[116:117], off offset:4
	v_lshlrev_b64 v[116:117], 12, v[186:187]
	v_lshl_add_u64 v[116:117], v[184:185], 0, v[116:117]
	global_load_dwordx4 v[116:119], v[116:117], off nt
	v_lshrrev_b32_e32 v183, 4, v183
	v_bitop3_b32 v183, v183, v205, 3 bitop3:0x6c
	v_lshl_add_u32 v209, v205, 8, s5
	v_lshlrev_b32_e32 v183, 4, v183
	v_add_u32_e32 v216, v209, v183
	ds_write_b128 v216, v[132:135]
	v_bitop3_b32 v132, v222, v205, 4 bitop3:0x36
	v_lshlrev_b32_e32 v132, 4, v132
	v_add_u32_e32 v217, v209, v132
	ds_write_b128 v217, v[128:131]
	v_bitop3_b32 v128, v222, v205, 8 bitop3:0x36
	v_lshlrev_b32_e32 v128, 4, v128
	v_add_u32_e32 v218, v209, v128
	ds_write_b128 v218, v[124:127]
	v_bitop3_b32 v124, v222, v205, 12 bitop3:0x36
	v_lshlrev_b32_e32 v124, 4, v124
	v_add_u32_e32 v219, v209, v124
	ds_write_b128 v219, v[120:123]
	v_lshl_add_u32 v120, v222, 8, s5
	v_and_b32_e32 v121, 64, v214
	v_add_u32_e32 v220, v120, v183
	v_xor_b32_e32 v120, 8, v214
	v_add_u32_e32 v125, 64, v121
	v_cmp_lt_i32_e64 s[0:1], v120, v125
	s_waitcnt lgkmcnt(0)
	v_cmp_eq_u32_e32 vcc, 0, v205
	v_xor_b32_e32 v126, 4, v214
	v_cndmask_b32_e64 v120, v214, v120, s[0:1]
	v_lshlrev_b32_e32 v205, 2, v120
	ds_read_b128 v[120:123], v220
	s_waitcnt vmcnt(0)
	v_pk_mul_f32 v[178:179], v[178:179], s[14:15] op_sel_hi:[1,0]
	v_cmp_lt_i32_e64 s[0:1], v126, v125
	v_pk_mul_f32 v[180:181], v[180:181], s[14:15] op_sel_hi:[1,0]
	v_xor_b32_e32 v129, 2, v214
	s_waitcnt lgkmcnt(0)
	v_pk_mul_f32 v[120:121], v[182:183], v[120:121] op_sel_hi:[0,1]
	v_cndmask_b32_e64 v126, v214, v126, s[0:1]
	v_pk_mul_f32 v[122:123], v[182:183], v[122:123] op_sel_hi:[0,1]
	v_lshlrev_b32_e32 v209, 2, v126
	v_cmp_lt_i32_e64 s[0:1], v129, v125
	s_lshl_b32 s22, s4, 2
	s_mov_b32 s23, s9
	v_cndmask_b32_e64 v129, v214, v129, s[0:1]
	v_lshlrev_b32_e32 v213, 2, v129
	v_xor_b32_e32 v129, 1, v214
	v_cmp_lt_i32_e64 s[0:1], v129, v125
	v_lshlrev_b32_e32 v182, 2, v221
	v_pk_fma_f32 v[120:121], v[178:179], v[120:121], v[224:225]
	v_pk_fma_f32 v[122:123], v[180:181], v[122:123], v[226:227]
	v_pk_mul_f32 v[126:127], v[120:121], v[120:121]
	v_pk_mul_f32 v[130:131], v[122:123], v[122:123]
	v_add_f32_e32 v126, v126, v127
	v_add_f32_e32 v126, v130, v126
	v_add_f32_e32 v126, v131, v126
	ds_bpermute_b32 v127, v205, v126
	v_cndmask_b32_e64 v125, v214, v129, s[0:1]
	v_lshlrev_b32_e32 v215, 2, v125
	v_mov_b32_e32 v131, v3
	s_waitcnt lgkmcnt(0)
	v_add_f32_e32 v127, v126, v127
	ds_bpermute_b32 v130, v209, v127
	v_cvt_pk_bf16_f32 v126, v120, v121
	v_lshlrev_b64 v[120:121], 11, v[176:177]
	s_waitcnt lgkmcnt(0)
	v_add_f32_e32 v125, v127, v130
	ds_bpermute_b32 v129, v213, v125
	v_cvt_pk_bf16_f32 v127, v122, v123
	v_lshl_add_u64 v[122:123], s[24:25], 0, v[120:121]
	v_lshlrev_b32_e32 v130, 1, v2
	v_lshl_add_u64 v[122:123], v[122:123], 0, v[130:131]
	s_waitcnt lgkmcnt(0)
	v_add_f32_e32 v120, v125, v129
	ds_bpermute_b32 v121, v215, v120
	global_store_dwordx2 v[122:123], v[126:127], off
	s_and_saveexec_b64 s[0:1], vcc
	s_cbranch_execz .LBB0_535
	v_lshlrev_b64 v[122:123], 6, v[176:177]
	v_lshl_add_u64 v[122:123], s[6:7], 0, v[122:123]
	v_lshl_add_u64 v[122:123], s[22:23], 2, v[122:123]
	v_mov_b32_e32 v183, v3
	v_lshl_add_u64 v[122:123], v[122:123], 0, v[182:183]
	s_waitcnt lgkmcnt(0)
	v_add_f32_e32 v120, v120, v121
	global_store_dword v[122:123], v120, off

; __device__ __forceinline__ uint2 pack4(f32x4 v) { uint2 r; r.x = pack2(v[0], v[1]); r.y = pack2(v[2], v[3]); return r; }
;     __device__ __forceinline__ void epilogue(f32x4 (&acc)[8][4], const Desc& d, unsigned char* stg) const {
;     ...
; #pragma unroll
;                 for (int i2 = 0; i2 < 4; ++i2) { xn[i2] = *(const float4*)(p.x + (rowb + (m + 1) * 16 + i2 * 4) * D + col); fn[i2] = p.rs[rowb + (m + 1) * 16 + i2 * 4].y; }
;             }
; #pragma unroll
;             for (int n = 0; n < 4; ++n) stgf_put(stg, n, acc[m][n], l15, gq);
;             asm volatile("s_waitcnt lgkmcnt(0)" ::: "memory");
; #pragma unroll
;             for (int i2 = 0; i2 < 4; ++i2) {
;                 const int rl = i2 * 4 + rsub;
;                 const size_t row = rowb + m * 16 + i2 * 4;
;                 const f32x4 v = stgf_get(stg, rl, c);
;                 const float fsm = fc[i2];
;                 const float4 xv = xc[i2];
;                 float4 r;
;                 r.x = xv.x + g1.x * (v[0] * fsm); r.y = xv.y + g1.y * (v[1] * fsm); r.z = xv.z + g1.z * (v[2] * fsm); r.w = xv.w + g1.w * (v[3] * fsm);
;                 *(uint2*)(p.x1 + row * D + col) = pack4((f32x4){r.x, r.y, r.z, r.w});
;                 float ss = r.x * r.x + r.y * r.y + r.z * r.z + r.w * r.w;
;                 ss += __shfl_xor(ss, 8); ss += __shfl_xor(ss, 4); ss += __shfl_xor(ss, 2); ss += __shfl_xor(ss, 1);
;                 if (c == 0) p.st2[row * 16 + nt * 4 + wc] = ss;
;             }
.LBB0_541:
	s_or_b64 exec, exec, s[0:1]
	v_or_b32_e32 v200, 32, v176
	v_mov_b32_e32 v201, v177
	s_waitcnt lgkmcnt(0)
	v_lshlrev_b64 v[120:121], 12, v[200:201]
	s_waitcnt lgkmcnt(0)
	v_lshl_add_u64 v[120:121], v[184:185], 0, v[120:121]
	v_or_b32_e32 v148, 44, v176
	v_mov_b32_e32 v149, v177
	global_load_dwordx4 v[132:135], v[120:121], off nt
	v_lshl_add_u64 v[120:121], v[200:201], 3, s[10:11]
	v_or_b32_e32 v156, 36, v176
	v_mov_b32_e32 v157, v177
	v_lshl_add_u64 v[206:207], v[148:149], 3, s[10:11]
	global_load_dword v204, v[120:121], off offset:4
	global_load_dword v150, v[206:207], off offset:4
	v_lshlrev_b64 v[120:121], 12, v[156:157]
	v_lshl_add_u64 v[120:121], v[184:185], 0, v[120:121]
	global_load_dwordx4 v[128:131], v[120:121], off nt
	v_lshl_add_u64 v[120:121], v[156:157], 3, s[10:11]
	v_or_b32_e32 v152, 40, v176
	v_mov_b32_e32 v153, v177
	global_load_dword v158, v[120:121], off offset:4
	v_lshlrev_b64 v[120:121], 12, v[152:153]
	v_lshl_add_u64 v[120:121], v[184:185], 0, v[120:121]
	global_load_dwordx4 v[124:127], v[120:121], off nt
	v_lshl_add_u64 v[120:121], v[152:153], 3, s[10:11]
	global_load_dword v154, v[120:121], off offset:4
	v_lshlrev_b64 v[120:121], 12, v[148:149]
	v_lshl_add_u64 v[120:121], v[184:185], 0, v[120:121]
	global_load_dwordx4 v[120:123], v[120:121], off nt
	ds_write_b128 v216, v[100:103]
	ds_write_b128 v217, v[104:107]
	ds_write_b128 v218, v[108:111]
	ds_write_b128 v219, v[112:115]
	s_waitcnt lgkmcnt(0)
	ds_read_b128 v[100:103], v220
	s_waitcnt lgkmcnt(0)
	v_pk_mul_f32 v[100:101], v[202:203], v[100:101] op_sel_hi:[0,1]
	v_pk_fma_f32 v[100:101], v[178:179], v[100:101], v[144:145]
	v_pk_mul_f32 v[102:103], v[202:203], v[102:103] op_sel_hi:[0,1]
	v_pk_fma_f32 v[102:103], v[180:181], v[102:103], v[146:147]
	v_pk_mul_f32 v[104:105], v[100:101], v[100:101]
	v_pk_mul_f32 v[106:107], v[102:103], v[102:103]
	v_add_f32_e32 v104, v104, v105
	v_add_f32_e32 v104, v106, v104
	v_add_f32_e32 v104, v107, v104
	ds_bpermute_b32 v105, v205, v104
	s_waitcnt lgkmcnt(0)
	v_add_f32_e32 v104, v104, v105
	ds_bpermute_b32 v105, v209, v104
	s_waitcnt lgkmcnt(0)
	v_add_f32_e32 v106, v104, v105
	ds_bpermute_b32 v107, v213, v106
	v_cvt_pk_bf16_f32 v104, v100, v101
	v_cvt_pk_bf16_f32 v105, v102, v103
	v_lshlrev_b64 v[102:103], 11, v[198:199]
	v_lshl_add_u64 v[102:103], s[24:25], 0, v[102:103]
	s_waitcnt lgkmcnt(0)
	v_add_f32_e32 v100, v106, v107
	ds_bpermute_b32 v101, v215, v100
	v_lshl_add_u64 v[102:103], v[102:103], 0, v[2:3]
	global_store_dwordx2 v[102:103], v[104:105], off
	s_and_saveexec_b64 s[0:1], vcc
	s_cbranch_execz .LBB0_543
	v_lshlrev_b64 v[102:103], 6, v[198:199]
	v_lshl_add_u64 v[102:103], s[6:7], 0, v[102:103]
	v_lshl_add_u64 v[102:103], s[22:23], 2, v[102:103]
	v_mov_b32_e32 v183, v3
	v_lshl_add_u64 v[102:103], v[102:103], 0, v[182:183]
	s_waitcnt lgkmcnt(0)
	v_add_f32_e32 v100, v100, v101
	global_store_dword v[102:103], v100, off

; __device__ __forceinline__ uint2 pack4(f32x4 v) { uint2 r; r.x = pack2(v[0], v[1]); r.y = pack2(v[2], v[3]); return r; }
;     __device__ __forceinline__ void epilogue(f32x4 (&acc)[8][4], const Desc& d, unsigned char* stg) const {
;     ...
; #pragma unroll
;                 for (int i2 = 0; i2 < 4; ++i2) { xn[i2] = *(const float4*)(p.x + (rowb + (m + 1) * 16 + i2 * 4) * D + col); fn[i2] = p.rs[rowb + (m + 1) * 16 + i2 * 4].y; }
;             }
; #pragma unroll
;             for (int n = 0; n < 4; ++n) stgf_put(stg, n, acc[m][n], l15, gq);
;             asm volatile("s_waitcnt lgkmcnt(0)" ::: "memory");
; #pragma unroll
;             for (int i2 = 0; i2 < 4; ++i2) {
;                 const int rl = i2 * 4 + rsub;
;                 const size_t row = rowb + m * 16 + i2 * 4;
;                 const f32x4 v = stgf_get(stg, rl, c);
;                 const float fsm = fc[i2];
;                 const float4 xv = xc[i2];
;                 float4 r;
;                 r.x = xv.x + g1.x * (v[0] * fsm); r.y = xv.y + g1.y * (v[1] * fsm); r.z = xv.z + g1.z * (v[2] * fsm); r.w = xv.w + g1.w * (v[3] * fsm);
;                 *(uint2*)(p.x1 + row * D + col) = pack4((f32x4){r.x, r.y, r.z, r.w});
;                 float ss = r.x * r.x + r.y * r.y + r.z * r.z + r.w * r.w;
;                 ss += __shfl_xor(ss, 8); ss += __shfl_xor(ss, 4); ss += __shfl_xor(ss, 2); ss += __shfl_xor(ss, 1);
;                 if (c == 0) p.st2[row * 16 + nt * 4 + wc] = ss;
;             }
.LBB0_549:
	s_or_b64 exec, exec, s[0:1]
	v_or_b32_e32 v146, 48, v176
	v_mov_b32_e32 v147, v177
	s_waitcnt lgkmcnt(0)
	v_lshlrev_b64 v[100:101], 12, v[146:147]
	s_waitcnt lgkmcnt(0)
	v_lshl_add_u64 v[100:101], v[184:185], 0, v[100:101]
	v_or_b32_e32 v118, 60, v176
	v_mov_b32_e32 v119, v177
	global_load_dwordx4 v[112:115], v[100:101], off nt
	v_lshl_add_u64 v[100:101], v[146:147], 3, s[10:11]
	v_or_b32_e32 v142, 52, v176
	v_mov_b32_e32 v143, v177
	v_lshl_add_u64 v[116:117], v[118:119], 3, s[10:11]
	global_load_dword v186, v[100:101], off offset:4
	global_load_dword v136, v[116:117], off offset:4
	v_lshlrev_b64 v[100:101], 12, v[142:143]
	v_lshl_add_u64 v[100:101], v[184:185], 0, v[100:101]
	global_load_dwordx4 v[108:111], v[100:101], off nt
	v_lshl_add_u64 v[100:101], v[142:143], 3, s[10:11]
	v_or_b32_e32 v138, 56, v176
	v_mov_b32_e32 v139, v177
	global_load_dword v144, v[100:101], off offset:4
	v_lshlrev_b64 v[100:101], 12, v[138:139]
	v_lshl_add_u64 v[100:101], v[184:185], 0, v[100:101]
	global_load_dwordx4 v[104:107], v[100:101], off nt
	v_lshl_add_u64 v[100:101], v[138:139], 3, s[10:11]
	global_load_dword v140, v[100:101], off offset:4
	v_lshlrev_b64 v[100:101], 12, v[118:119]
	v_lshl_add_u64 v[100:101], v[184:185], 0, v[100:101]
	global_load_dwordx4 v[100:103], v[100:101], off nt
	ds_write_b128 v216, v[84:87]
	ds_write_b128 v217, v[88:91]
	ds_write_b128 v218, v[92:95]
	ds_write_b128 v219, v[96:99]
	s_waitcnt lgkmcnt(0)
	ds_read_b128 v[84:87], v220
	s_waitcnt vmcnt(18) lgkmcnt(0)
	v_pk_mul_f32 v[84:85], v[204:205], v[84:85] op_sel_hi:[0,1]
	v_pk_fma_f32 v[84:85], v[178:179], v[84:85], v[132:133]
	v_pk_mul_f32 v[86:87], v[204:205], v[86:87] op_sel_hi:[0,1]
	v_pk_fma_f32 v[86:87], v[180:181], v[86:87], v[134:135]
	v_pk_mul_f32 v[88:89], v[84:85], v[84:85]
	v_pk_mul_f32 v[90:91], v[86:87], v[86:87]
	v_add_f32_e32 v88, v88, v89
	v_add_f32_e32 v88, v90, v88
	v_add_f32_e32 v88, v91, v88
	ds_bpermute_b32 v89, v205, v88
	s_waitcnt lgkmcnt(0)
	v_add_f32_e32 v88, v88, v89
	ds_bpermute_b32 v89, v209, v88
	s_waitcnt lgkmcnt(0)
	v_add_f32_e32 v90, v88, v89
	ds_bpermute_b32 v91, v213, v90
	v_cvt_pk_bf16_f32 v88, v84, v85
	v_cvt_pk_bf16_f32 v89, v86, v87
	v_lshlrev_b64 v[86:87], 11, v[200:201]
	v_lshl_add_u64 v[86:87], s[24:25], 0, v[86:87]
	s_waitcnt lgkmcnt(0)
	v_add_f32_e32 v84, v90, v91
	ds_bpermute_b32 v85, v215, v84
	v_lshl_add_u64 v[86:87], v[86:87], 0, v[2:3]
	global_store_dwordx2 v[86:87], v[88:89], off
	s_and_saveexec_b64 s[0:1], vcc
	s_cbranch_execz .LBB0_551
	v_lshlrev_b64 v[86:87], 6, v[200:201]
	v_lshl_add_u64 v[86:87], s[6:7], 0, v[86:87]
	v_lshl_add_u64 v[86:87], s[22:23], 2, v[86:87]
	v_mov_b32_e32 v183, v3
	v_lshl_add_u64 v[86:87], v[86:87], 0, v[182:183]
	s_waitcnt lgkmcnt(0)
	v_add_f32_e32 v84, v84, v85
	global_store_dword v[86:87], v84, off

; __device__ __forceinline__ uint2 pack4(f32x4 v) { uint2 r; r.x = pack2(v[0], v[1]); r.y = pack2(v[2], v[3]); return r; }
;     __device__ __forceinline__ void epilogue(f32x4 (&acc)[8][4], const Desc& d, unsigned char* stg) const {
;     ...
; #pragma unroll
;                 for (int i2 = 0; i2 < 4; ++i2) { xn[i2] = *(const float4*)(p.x + (rowb + (m + 1) * 16 + i2 * 4) * D + col); fn[i2] = p.rs[rowb + (m + 1) * 16 + i2 * 4].y; }
;             }
; #pragma unroll
;             for (int n = 0; n < 4; ++n) stgf_put(stg, n, acc[m][n], l15, gq);
;             asm volatile("s_waitcnt lgkmcnt(0)" ::: "memory");
; #pragma unroll
;             for (int i2 = 0; i2 < 4; ++i2) {
;                 const int rl = i2 * 4 + rsub;
;                 const size_t row = rowb + m * 16 + i2 * 4;
;                 const f32x4 v = stgf_get(stg, rl, c);
;                 const float fsm = fc[i2];
;                 const float4 xv = xc[i2];
;                 float4 r;
;                 r.x = xv.x + g1.x * (v[0] * fsm); r.y = xv.y + g1.y * (v[1] * fsm); r.z = xv.z + g1.z * (v[2] * fsm); r.w = xv.w + g1.w * (v[3] * fsm);
;                 *(uint2*)(p.x1 + row * D + col) = pack4((f32x4){r.x, r.y, r.z, r.w});
;                 float ss = r.x * r.x + r.y * r.y + r.z * r.z + r.w * r.w;
;                 ss += __shfl_xor(ss, 8); ss += __shfl_xor(ss, 4); ss += __shfl_xor(ss, 2); ss += __shfl_xor(ss, 1);
;                 if (c == 0) p.st2[row * 16 + nt * 4 + wc] = ss;
;             }
.LBB0_557:
	s_or_b64 exec, exec, s[0:1]
	v_or_b32_e32 v130, 64, v176
	v_mov_b32_e32 v131, v177
	s_waitcnt lgkmcnt(0)
	v_lshlrev_b64 v[84:85], 12, v[130:131]
	s_waitcnt lgkmcnt(0)
	v_lshl_add_u64 v[84:85], v[184:185], 0, v[84:85]
	v_or_b32_e32 v116, 0x4c, v176
	v_mov_b32_e32 v117, v177
	global_load_dwordx4 v[96:99], v[84:85], off nt
	v_lshl_add_u64 v[84:85], v[130:131], 3, s[10:11]
	v_or_b32_e32 v126, 0x44, v176
	v_mov_b32_e32 v127, v177
	v_lshl_add_u64 v[120:121], v[116:117], 3, s[10:11]
	global_load_dword v132, v[84:85], off offset:4
	v_or_b32_e32 v122, 0x48, v176
	global_load_dword v120, v[120:121], off offset:4
	v_lshlrev_b64 v[84:85], 12, v[126:127]
	v_lshl_add_u64 v[84:85], v[184:185], 0, v[84:85]
	global_load_dwordx4 v[92:95], v[84:85], off nt
	v_lshl_add_u64 v[84:85], v[126:127], 3, s[10:11]
	v_mov_b32_e32 v123, v177
	global_load_dword v128, v[84:85], off offset:4
	v_lshlrev_b64 v[84:85], 12, v[122:123]
	v_lshl_add_u64 v[84:85], v[184:185], 0, v[84:85]
	global_load_dwordx4 v[88:91], v[84:85], off nt
	v_lshl_add_u64 v[84:85], v[122:123], 3, s[10:11]
	global_load_dword v124, v[84:85], off offset:4
	v_lshlrev_b64 v[84:85], 12, v[116:117]
	v_lshl_add_u64 v[84:85], v[184:185], 0, v[84:85]
	global_load_dwordx4 v[84:87], v[84:85], off nt
	ds_write_b128 v216, v[68:71]
	ds_write_b128 v217, v[72:75]
	ds_write_b128 v218, v[76:79]
	ds_write_b128 v219, v[80:83]
	s_waitcnt lgkmcnt(0)
	ds_read_b128 v[68:71], v220
	s_waitcnt vmcnt(18) lgkmcnt(0)
	v_pk_mul_f32 v[68:69], v[186:187], v[68:69] op_sel_hi:[0,1]
	v_pk_fma_f32 v[68:69], v[178:179], v[68:69], v[112:113]
	v_pk_mul_f32 v[70:71], v[186:187], v[70:71] op_sel_hi:[0,1]
	v_pk_fma_f32 v[70:71], v[180:181], v[70:71], v[114:115]
	v_pk_mul_f32 v[72:73], v[68:69], v[68:69]
	v_pk_mul_f32 v[74:75], v[70:71], v[70:71]
	v_add_f32_e32 v72, v72, v73
	v_add_f32_e32 v72, v74, v72
	v_add_f32_e32 v72, v75, v72
	ds_bpermute_b32 v73, v205, v72
	s_waitcnt lgkmcnt(0)
	v_add_f32_e32 v72, v72, v73
	ds_bpermute_b32 v73, v209, v72
	s_waitcnt lgkmcnt(0)
	v_add_f32_e32 v74, v72, v73
	ds_bpermute_b32 v75, v213, v74
	v_cvt_pk_bf16_f32 v72, v68, v69
	v_cvt_pk_bf16_f32 v73, v70, v71
	v_lshlrev_b64 v[70:71], 11, v[146:147]
	v_lshl_add_u64 v[70:71], s[24:25], 0, v[70:71]
	s_waitcnt lgkmcnt(0)
	v_add_f32_e32 v68, v74, v75
	ds_bpermute_b32 v69, v215, v68
	v_lshl_add_u64 v[70:71], v[70:71], 0, v[2:3]
	global_store_dwordx2 v[70:71], v[72:73], off
	s_and_saveexec_b64 s[0:1], vcc
	s_cbranch_execz .LBB0_559
	v_lshlrev_b64 v[70:71], 6, v[146:147]
	v_lshl_add_u64 v[70:71], s[6:7], 0, v[70:71]
	v_lshl_add_u64 v[70:71], s[22:23], 2, v[70:71]
	v_mov_b32_e32 v183, v3
	v_lshl_add_u64 v[70:71], v[70:71], 0, v[182:183]
	s_waitcnt lgkmcnt(0)
	v_add_f32_e32 v68, v68, v69
	global_store_dword v[70:71], v68, off

; __device__ __forceinline__ uint2 pack4(f32x4 v) { uint2 r; r.x = pack2(v[0], v[1]); r.y = pack2(v[2], v[3]); return r; }
;     __device__ __forceinline__ void epilogue(f32x4 (&acc)[8][4], const Desc& d, unsigned char* stg) const {
;     ...
; #pragma unroll
;                 for (int i2 = 0; i2 < 4; ++i2) { xn[i2] = *(const float4*)(p.x + (rowb + (m + 1) * 16 + i2 * 4) * D + col); fn[i2] = p.rs[rowb + (m + 1) * 16 + i2 * 4].y; }
;             }
; #pragma unroll
;             for (int n = 0; n < 4; ++n) stgf_put(stg, n, acc[m][n], l15, gq);
;             asm volatile("s_waitcnt lgkmcnt(0)" ::: "memory");
; #pragma unroll
;             for (int i2 = 0; i2 < 4; ++i2) {
;                 const int rl = i2 * 4 + rsub;
;                 const size_t row = rowb + m * 16 + i2 * 4;
;                 const f32x4 v = stgf_get(stg, rl, c);
;                 const float fsm = fc[i2];
;                 const float4 xv = xc[i2];
;                 float4 r;
;                 r.x = xv.x + g1.x * (v[0] * fsm); r.y = xv.y + g1.y * (v[1] * fsm); r.z = xv.z + g1.z * (v[2] * fsm); r.w = xv.w + g1.w * (v[3] * fsm);
;                 *(uint2*)(p.x1 + row * D + col) = pack4((f32x4){r.x, r.y, r.z, r.w});
;                 float ss = r.x * r.x + r.y * r.y + r.z * r.z + r.w * r.w;
;                 ss += __shfl_xor(ss, 8); ss += __shfl_xor(ss, 4); ss += __shfl_xor(ss, 2); ss += __shfl_xor(ss, 1);
;                 if (c == 0) p.st2[row * 16 + nt * 4 + wc] = ss;
;             }
.LBB0_565:
	s_or_b64 exec, exec, s[0:1]
	v_or_b32_e32 v112, 0x50, v176
	v_mov_b32_e32 v113, v177
	s_waitcnt lgkmcnt(0)
	v_lshlrev_b64 v[68:69], 12, v[112:113]
	s_waitcnt lgkmcnt(0)
	v_lshl_add_u64 v[68:69], v[184:185], 0, v[68:69]
	v_or_b32_e32 v100, 0x5c, v176
	v_mov_b32_e32 v101, v177
	global_load_dwordx4 v[80:83], v[68:69], off nt
	v_lshl_add_u64 v[68:69], v[112:113], 3, s[10:11]
	v_or_b32_e32 v108, 0x54, v176
	v_mov_b32_e32 v109, v177
	v_lshl_add_u64 v[102:103], v[100:101], 3, s[10:11]
	global_load_dword v114, v[68:69], off offset:4
	v_or_b32_e32 v104, 0x58, v176
	global_load_dword v102, v[102:103], off offset:4
	v_lshlrev_b64 v[68:69], 12, v[108:109]
	v_lshl_add_u64 v[68:69], v[184:185], 0, v[68:69]
	global_load_dwordx4 v[76:79], v[68:69], off nt
	v_lshl_add_u64 v[68:69], v[108:109], 3, s[10:11]
	v_mov_b32_e32 v105, v177
	global_load_dword v110, v[68:69], off offset:4
	v_lshlrev_b64 v[68:69], 12, v[104:105]
	v_lshl_add_u64 v[68:69], v[184:185], 0, v[68:69]
	global_load_dwordx4 v[72:75], v[68:69], off nt
	v_lshl_add_u64 v[68:69], v[104:105], 3, s[10:11]
	global_load_dword v106, v[68:69], off offset:4
	v_lshlrev_b64 v[68:69], 12, v[100:101]
	v_lshl_add_u64 v[68:69], v[184:185], 0, v[68:69]
	global_load_dwordx4 v[68:71], v[68:69], off nt
	ds_write_b128 v216, v[52:55]
	ds_write_b128 v217, v[56:59]
	ds_write_b128 v218, v[60:63]
	ds_write_b128 v219, v[64:67]
	s_waitcnt lgkmcnt(0)
	ds_read_b128 v[52:55], v220
	s_waitcnt vmcnt(18) lgkmcnt(0)
	v_pk_mul_f32 v[52:53], v[132:133], v[52:53] op_sel_hi:[0,1]
	v_pk_fma_f32 v[52:53], v[178:179], v[52:53], v[96:97]
	v_pk_mul_f32 v[54:55], v[132:133], v[54:55] op_sel_hi:[0,1]
	v_pk_fma_f32 v[54:55], v[180:181], v[54:55], v[98:99]
	v_pk_mul_f32 v[56:57], v[52:53], v[52:53]
	v_pk_mul_f32 v[58:59], v[54:55], v[54:55]
	v_add_f32_e32 v56, v56, v57
	v_add_f32_e32 v56, v58, v56
	v_add_f32_e32 v56, v59, v56
	ds_bpermute_b32 v57, v205, v56
	s_waitcnt lgkmcnt(0)
	v_add_f32_e32 v56, v56, v57
	ds_bpermute_b32 v57, v209, v56
	s_waitcnt lgkmcnt(0)
	v_add_f32_e32 v58, v56, v57
	ds_bpermute_b32 v59, v213, v58
	v_cvt_pk_bf16_f32 v56, v52, v53
	v_cvt_pk_bf16_f32 v57, v54, v55
	v_lshlrev_b64 v[54:55], 11, v[130:131]
	v_lshl_add_u64 v[54:55], s[24:25], 0, v[54:55]
	s_waitcnt lgkmcnt(0)
	v_add_f32_e32 v52, v58, v59
	ds_bpermute_b32 v53, v215, v52
	v_lshl_add_u64 v[54:55], v[54:55], 0, v[2:3]
	global_store_dwordx2 v[54:55], v[56:57], off
	s_and_saveexec_b64 s[0:1], vcc
	s_cbranch_execz .LBB0_567
	v_lshlrev_b64 v[54:55], 6, v[130:131]
	v_lshl_add_u64 v[54:55], s[6:7], 0, v[54:55]
	v_lshl_add_u64 v[54:55], s[22:23], 2, v[54:55]
	v_mov_b32_e32 v183, v3
	v_lshl_add_u64 v[54:55], v[54:55], 0, v[182:183]
	s_waitcnt lgkmcnt(0)
	v_add_f32_e32 v52, v52, v53
	global_store_dword v[54:55], v52, off

; __device__ __forceinline__ uint2 pack4(f32x4 v) { uint2 r; r.x = pack2(v[0], v[1]); r.y = pack2(v[2], v[3]); return r; }
;     __device__ __forceinline__ void epilogue(f32x4 (&acc)[8][4], const Desc& d, unsigned char* stg) const {
;     ...
; #pragma unroll
;                 for (int i2 = 0; i2 < 4; ++i2) { xn[i2] = *(const float4*)(p.x + (rowb + (m + 1) * 16 + i2 * 4) * D + col); fn[i2] = p.rs[rowb + (m + 1) * 16 + i2 * 4].y; }
;             }
; #pragma unroll
;             for (int n = 0; n < 4; ++n) stgf_put(stg, n, acc[m][n], l15, gq);
;             asm volatile("s_waitcnt lgkmcnt(0)" ::: "memory");
; #pragma unroll
;             for (int i2 = 0; i2 < 4; ++i2) {
;                 const int rl = i2 * 4 + rsub;
;                 const size_t row = rowb + m * 16 + i2 * 4;
;                 const f32x4 v = stgf_get(stg, rl, c);
;                 const float fsm = fc[i2];
;                 const float4 xv = xc[i2];
;                 float4 r;
;                 r.x = xv.x + g1.x * (v[0] * fsm); r.y = xv.y + g1.y * (v[1] * fsm); r.z = xv.z + g1.z * (v[2] * fsm); r.w = xv.w + g1.w * (v[3] * fsm);
;                 *(uint2*)(p.x1 + row * D + col) = pack4((f32x4){r.x, r.y, r.z, r.w});
;                 float ss = r.x * r.x + r.y * r.y + r.z * r.z + r.w * r.w;
;                 ss += __shfl_xor(ss, 8); ss += __shfl_xor(ss, 4); ss += __shfl_xor(ss, 2); ss += __shfl_xor(ss, 1);
;                 if (c == 0) p.st2[row * 16 + nt * 4 + wc] = ss;
;             }
.LBB0_573:
	s_or_b64 exec, exec, s[0:1]
	v_or_b32_e32 v96, 0x60, v176
	v_mov_b32_e32 v97, v177
	s_waitcnt lgkmcnt(0)
	v_lshlrev_b64 v[52:53], 12, v[96:97]
	s_waitcnt lgkmcnt(0)
	v_lshl_add_u64 v[52:53], v[184:185], 0, v[52:53]
	v_or_b32_e32 v84, 0x6c, v176
	v_mov_b32_e32 v85, v177
	global_load_dwordx4 v[64:67], v[52:53], off nt
	v_lshl_add_u64 v[52:53], v[96:97], 3, s[10:11]
	v_or_b32_e32 v92, 0x64, v176
	v_mov_b32_e32 v93, v177
	v_lshl_add_u64 v[86:87], v[84:85], 3, s[10:11]
	global_load_dword v98, v[52:53], off offset:4
	v_or_b32_e32 v88, 0x68, v176
	global_load_dword v86, v[86:87], off offset:4
	v_lshlrev_b64 v[52:53], 12, v[92:93]
	v_lshl_add_u64 v[52:53], v[184:185], 0, v[52:53]
	global_load_dwordx4 v[60:63], v[52:53], off nt
	v_lshl_add_u64 v[52:53], v[92:93], 3, s[10:11]
	v_mov_b32_e32 v89, v177
	global_load_dword v94, v[52:53], off offset:4
	v_lshlrev_b64 v[52:53], 12, v[88:89]
	v_lshl_add_u64 v[52:53], v[184:185], 0, v[52:53]
	global_load_dwordx4 v[56:59], v[52:53], off nt
	v_lshl_add_u64 v[52:53], v[88:89], 3, s[10:11]
	global_load_dword v90, v[52:53], off offset:4
	v_lshlrev_b64 v[52:53], 12, v[84:85]
	v_lshl_add_u64 v[52:53], v[184:185], 0, v[52:53]
	global_load_dwordx4 v[52:55], v[52:53], off nt
	ds_write_b128 v216, v[36:39]
	ds_write_b128 v217, v[40:43]
	ds_write_b128 v218, v[44:47]
	ds_write_b128 v219, v[48:51]
	s_waitcnt lgkmcnt(0)
	ds_read_b128 v[36:39], v220
	s_waitcnt vmcnt(18) lgkmcnt(0)
	v_pk_mul_f32 v[36:37], v[114:115], v[36:37] op_sel_hi:[0,1]
	v_pk_fma_f32 v[36:37], v[178:179], v[36:37], v[80:81]
	v_pk_mul_f32 v[38:39], v[114:115], v[38:39] op_sel_hi:[0,1]
	v_pk_fma_f32 v[38:39], v[180:181], v[38:39], v[82:83]
	v_pk_mul_f32 v[40:41], v[36:37], v[36:37]
	v_pk_mul_f32 v[42:43], v[38:39], v[38:39]
	v_add_f32_e32 v40, v40, v41
	v_add_f32_e32 v40, v42, v40
	v_add_f32_e32 v40, v43, v40
	ds_bpermute_b32 v41, v205, v40
	s_waitcnt lgkmcnt(0)
	v_add_f32_e32 v40, v40, v41
	ds_bpermute_b32 v41, v209, v40
	s_waitcnt lgkmcnt(0)
	v_add_f32_e32 v42, v40, v41
	ds_bpermute_b32 v43, v213, v42
	v_cvt_pk_bf16_f32 v40, v36, v37
	v_cvt_pk_bf16_f32 v41, v38, v39
	v_lshlrev_b64 v[38:39], 11, v[112:113]
	v_lshl_add_u64 v[38:39], s[24:25], 0, v[38:39]
	s_waitcnt lgkmcnt(0)
	v_add_f32_e32 v36, v42, v43
	ds_bpermute_b32 v37, v215, v36
	v_lshl_add_u64 v[38:39], v[38:39], 0, v[2:3]
	global_store_dwordx2 v[38:39], v[40:41], off
	s_and_saveexec_b64 s[0:1], vcc
	s_cbranch_execz .LBB0_575
	v_lshlrev_b64 v[38:39], 6, v[112:113]
	v_lshl_add_u64 v[38:39], s[6:7], 0, v[38:39]
	v_lshl_add_u64 v[38:39], s[22:23], 2, v[38:39]
	v_mov_b32_e32 v183, v3
	v_lshl_add_u64 v[38:39], v[38:39], 0, v[182:183]
	s_waitcnt lgkmcnt(0)
	v_add_f32_e32 v36, v36, v37
	global_store_dword v[38:39], v36, off

; __device__ __forceinline__ uint2 pack4(f32x4 v) { uint2 r; r.x = pack2(v[0], v[1]); r.y = pack2(v[2], v[3]); return r; }
;     __device__ __forceinline__ void epilogue(f32x4 (&acc)[8][4], const Desc& d, unsigned char* stg) const {
;     ...
; #pragma unroll
;                 for (int i2 = 0; i2 < 4; ++i2) { xn[i2] = *(const float4*)(p.x + (rowb + (m + 1) * 16 + i2 * 4) * D + col); fn[i2] = p.rs[rowb + (m + 1) * 16 + i2 * 4].y; }
;             }
; #pragma unroll
;             for (int n = 0; n < 4; ++n) stgf_put(stg, n, acc[m][n], l15, gq);
;             asm volatile("s_waitcnt lgkmcnt(0)" ::: "memory");
; #pragma unroll
;             for (int i2 = 0; i2 < 4; ++i2) {
;                 const int rl = i2 * 4 + rsub;
;                 const size_t row = rowb + m * 16 + i2 * 4;
;                 const f32x4 v = stgf_get(stg, rl, c);
;                 const float fsm = fc[i2];
;                 const float4 xv = xc[i2];
;                 float4 r;
;                 r.x = xv.x + g1.x * (v[0] * fsm); r.y = xv.y + g1.y * (v[1] * fsm); r.z = xv.z + g1.z * (v[2] * fsm); r.w = xv.w + g1.w * (v[3] * fsm);
;                 *(uint2*)(p.x1 + row * D + col) = pack4((f32x4){r.x, r.y, r.z, r.w});
;                 float ss = r.x * r.x + r.y * r.y + r.z * r.z + r.w * r.w;
;                 ss += __shfl_xor(ss, 8); ss += __shfl_xor(ss, 4); ss += __shfl_xor(ss, 2); ss += __shfl_xor(ss, 1);
;                 if (c == 0) p.st2[row * 16 + nt * 4 + wc] = ss;
;             }
.LBB0_581:
	s_or_b64 exec, exec, s[0:1]
	v_or_b32_e32 v78, 0x70, v176
	v_mov_b32_e32 v79, v177
	s_waitcnt lgkmcnt(0)
	v_lshlrev_b64 v[36:37], 12, v[78:79]
	s_waitcnt lgkmcnt(0)
	v_lshl_add_u64 v[36:37], v[184:185], 0, v[36:37]
	v_or_b32_e32 v74, 0x74, v176
	v_or_b32_e32 v70, 0x78, v176
	v_or_b32_e32 v176, 0x7c, v176
	global_load_dwordx4 v[48:51], v[36:37], off nt
	v_lshl_add_u64 v[36:37], v[78:79], 3, s[10:11]
	v_mov_b32_e32 v75, v177
	v_lshl_add_u64 v[68:69], v[176:177], 3, s[10:11]
	global_load_dword v80, v[36:37], off offset:4
	v_mov_b32_e32 v71, v177
	global_load_dword v68, v[68:69], off offset:4
	v_lshlrev_b64 v[36:37], 12, v[74:75]
	v_lshl_add_u64 v[36:37], v[184:185], 0, v[36:37]
	global_load_dwordx4 v[44:47], v[36:37], off nt
	v_lshl_add_u64 v[36:37], v[74:75], 3, s[10:11]
	global_load_dword v76, v[36:37], off offset:4
	v_lshlrev_b64 v[36:37], 12, v[70:71]
	v_lshl_add_u64 v[36:37], v[184:185], 0, v[36:37]
	global_load_dwordx4 v[40:43], v[36:37], off nt
	v_lshl_add_u64 v[36:37], v[70:71], 3, s[10:11]
	global_load_dword v72, v[36:37], off offset:4
	v_lshlrev_b64 v[36:37], 12, v[176:177]
	v_lshl_add_u64 v[36:37], v[184:185], 0, v[36:37]
	global_load_dwordx4 v[36:39], v[36:37], off nt
	ds_write_b128 v216, v[20:23]
	ds_write_b128 v217, v[24:27]
	ds_write_b128 v218, v[28:31]
	ds_write_b128 v219, v[32:35]
	s_waitcnt lgkmcnt(0)
	ds_read_b128 v[20:23], v220
	s_waitcnt vmcnt(18) lgkmcnt(0)
	v_pk_mul_f32 v[20:21], v[98:99], v[20:21] op_sel_hi:[0,1]
	v_pk_fma_f32 v[20:21], v[178:179], v[20:21], v[64:65]
	v_pk_mul_f32 v[22:23], v[98:99], v[22:23] op_sel_hi:[0,1]
	v_pk_fma_f32 v[22:23], v[180:181], v[22:23], v[66:67]
	v_pk_mul_f32 v[24:25], v[20:21], v[20:21]
	v_pk_mul_f32 v[26:27], v[22:23], v[22:23]
	v_add_f32_e32 v24, v24, v25
	v_add_f32_e32 v24, v26, v24
	v_add_f32_e32 v24, v27, v24
	ds_bpermute_b32 v25, v205, v24
	s_waitcnt lgkmcnt(0)
	v_add_f32_e32 v24, v24, v25
	ds_bpermute_b32 v25, v209, v24
	s_waitcnt lgkmcnt(0)
	v_add_f32_e32 v26, v24, v25
	ds_bpermute_b32 v27, v213, v26
	v_cvt_pk_bf16_f32 v24, v20, v21
	v_cvt_pk_bf16_f32 v25, v22, v23
	v_lshlrev_b64 v[22:23], 11, v[96:97]
	v_lshl_add_u64 v[22:23], s[24:25], 0, v[22:23]
	s_waitcnt lgkmcnt(0)
	v_add_f32_e32 v20, v26, v27
	ds_bpermute_b32 v21, v215, v20
	v_lshl_add_u64 v[22:23], v[22:23], 0, v[2:3]
	global_store_dwordx2 v[22:23], v[24:25], off
	s_and_saveexec_b64 s[0:1], vcc
	s_cbranch_execz .LBB0_583
	v_lshlrev_b64 v[22:23], 6, v[96:97]
	v_lshl_add_u64 v[22:23], s[6:7], 0, v[22:23]
	v_lshl_add_u64 v[22:23], s[22:23], 2, v[22:23]
	v_mov_b32_e32 v183, v3
	v_lshl_add_u64 v[22:23], v[22:23], 0, v[182:183]
	s_waitcnt lgkmcnt(0)
	v_add_f32_e32 v20, v20, v21
	global_store_dword v[22:23], v20, off

; __device__ __forceinline__ ConvJob conv_job_decode(const Params& p, int job, int tid) {
;     ...
;         const int q = job - 8192, e = q >> 4, ng = q & 15;
;         j.sp = p.we_down + (size_t)e * 262144 + (size_t)kr * 1024 + ng * 64 + n4; j.ldsrc = 1024;
;         j.dst8 = p.dT8 + (size_t)e * 262144 + (size_t)(ng * 64) * 256; j.ld8 = 256; j.s8 = D8S;
.LBB0_954:
	s_lshl_b32 s1, s14, 2
	s_mul_i32 s12, s14, 0x20c
	s_mov_b32 s13, 0
	s_sub_u32 s16, 0, s1
	v_lshl_add_u64 v[14:15], v[10:11], 0, s[12:13]
	s_subb_u32 s17, 0, 0
	v_lshl_add_u64 v[20:21], v[14:15], 0, s[16:17]
	v_lshl_add_u64 v[22:23], v[20:21], 0, s[16:17]
	v_lshl_add_u64 v[24:25], v[22:23], 0, s[16:17]
	v_mov_b32_e32 v9, 0xfffffe0c
	v_mad_i64_i32 v[16:17], s[14:15], s14, v9, v[24:25]
	global_load_dwordx4 v[26:29], v[16:17], off nt
	v_lshl_add_u64 v[16:17], v[16:17], 0, s[16:17]
	global_load_dwordx4 v[30:33], v[16:17], off nt
	v_lshl_add_u64 v[16:17], v[16:17], 0, s[16:17]
	global_load_dwordx4 v[34:37], v[10:11], off nt
	global_load_dwordx4 v[38:41], v[16:17], off nt
	global_load_dwordx4 v[42:45], v[22:23], off nt
	global_load_dwordx4 v[46:49], v[24:25], off nt
	global_load_dwordx4 v[50:53], v[14:15], off nt
	global_load_dwordx4 v[54:57], v[20:21], off nt
	s_mov_b32 s1, 0xc3dc0000
	v_mov_b32_e32 v23, 0x43dc0000
	v_mov_b32_e32 v14, 0
	v_mov_b32_e32 v15, 0
	v_ashrrev_i32_e32 v10, 4, v13
	s_waitcnt vmcnt(19)
	v_lshrrev_b32_e32 v58, 2, v8
	v_ashrrev_i32_e32 v19, 6, v13
	v_lshlrev_b32_e32 v59, 8, v8
	v_mov_b32_e32 v11, s47
	v_mov_b32_e32 v18, s45
	v_add_u32_e32 v21, 32, v10
	v_xor_b32_e32 v22, v58, v19
	v_lshlrev_b32_e32 v24, 2, v10
	v_xor_b32_e32 v25, 4, v58
	v_cmp_gt_u32_e32 vcc, 32, v8
	v_mov_b32_e32 v60, s46
	v_mov_b32_e32 v61, s44
	v_xor_b32_e32 v62, 8, v58
	v_xor_b32_e32 v63, 12, v58
	v_cndmask_b32_e32 v11, v11, v18, vcc
	v_and_b32_e32 v18, 12, v24
	v_xor_b32_e32 v24, v25, v19
	v_ashrrev_i32_e32 v21, 2, v21
	v_lshl_add_u32 v22, v22, 4, v59
	v_cndmask_b32_e32 v10, v60, v61, vcc
	v_xor_b32_e32 v60, v62, v19
	v_xor_b32_e32 v61, v63, v19
	v_xor_b32_e32 v58, v21, v58
	v_xor_b32_e32 v64, v25, v21
	v_xor_b32_e32 v62, v62, v21
	v_xor_b32_e32 v63, v63, v21
	v_or_b32_e32 v65, v22, v18
	v_lshl_add_u32 v21, v24, 4, v59
	v_mov_b32_e32 v20, 0
	v_or_b32_e32 v24, v21, v18
	v_lshl_add_u32 v25, v60, 4, v59
	v_or_b32_e32 v60, v25, v18
	v_lshrrev_b32_e32 v16, 3, v13
	v_and_b32_e32 v17, 7, v13
	v_lshl_add_u64 v[6:7], s[48:49], 0, v[6:7]
	s_mov_b64 s[16:17], 0
	v_mov_b32_e32 v9, 0
	s_and_b64 vcc, exec, s[8:9]
	v_lshlrev_b32_e32 v8, 2, v8
	s_waitcnt vmcnt(7)
	v_mul_f32_e32 v26, s5, v26
	v_mul_f32_e32 v27, s5, v27
	s_waitcnt vmcnt(6)
	v_mul_f32_e32 v30, s5, v30
	s_waitcnt vmcnt(5)
	v_mul_f32_e32 v34, s5, v34
	s_waitcnt vmcnt(4)
	v_mul_f32_e32 v38, s5, v38
	v_mul_f32_e32 v35, s5, v35
	v_mul_f32_e32 v39, s5, v39
	v_med3_f32 v34, v34, s1, v23
	v_med3_f32 v38, v38, s1, v23
	v_med3_f32 v35, v35, s1, v23
	v_med3_f32 v39, v39, s1, v23
	v_cvt_pk_fp8_f32 v14, v34, v38
	v_cvt_pk_fp8_f32 v15, v35, v39
	v_med3_f32 v26, v26, s1, v23
	v_mul_f32_e32 v31, s5, v31
	v_med3_f32 v30, v30, s1, v23
	v_med3_f32 v27, v27, s1, v23
	v_med3_f32 v31, v31, s1, v23
	v_cvt_pk_fp8_f32 v14, v30, v26 op_sel:[0,0,1]
	v_cvt_pk_fp8_f32 v15, v31, v27 op_sel:[0,0,1]
	v_mul_f32_e32 v36, s5, v36
	v_mul_f32_e32 v40, s5, v40
	v_mul_f32_e32 v37, s5, v37
	v_mul_f32_e32 v41, s5, v41
	v_med3_f32 v36, v36, s1, v23
	v_med3_f32 v40, v40, s1, v23
	v_med3_f32 v34, v37, s1, v23
	v_med3_f32 v26, v41, s1, v23
	ds_write_b32 v65, v14
	ds_write_b32 v24, v15 offset:256
	v_mov_b32_e32 v15, 0
	v_cvt_pk_fp8_f32 v20, v36, v40
	v_cvt_pk_fp8_f32 v15, v34, v26
	v_mul_f32_e32 v28, s5, v28
	v_mul_f32_e32 v32, s5, v32
	v_mul_f32_e32 v14, s5, v33
	v_mul_f32_e32 v24, s5, v29
	v_med3_f32 v28, v28, s1, v23
	v_med3_f32 v32, v32, s1, v23
	v_med3_f32 v14, v14, s1, v23
	v_med3_f32 v24, v24, s1, v23
	v_cvt_pk_fp8_f32 v20, v32, v28 op_sel:[0,0,1]
	v_cvt_pk_fp8_f32 v15, v14, v24 op_sel:[0,0,1]
	v_lshl_add_u32 v28, v61, 4, v59
	v_or_b32_e32 v14, v28, v18
	ds_write_b32 v60, v20 offset:512
	ds_write_b32 v14, v15 offset:768
	s_waitcnt vmcnt(2)
	v_mul_f32_e32 v14, s5, v46
	v_mul_f32_e32 v15, s5, v42
	v_med3_f32 v14, v14, s1, v23
	v_med3_f32 v15, v15, s1, v23
	v_mov_b32_e32 v24, 0
	v_cvt_pk_fp8_f32 v24, v14, v15
	s_waitcnt vmcnt(0)
	v_mul_f32_e32 v20, s5, v54
	v_mul_f32_e32 v15, s5, v50
	v_med3_f32 v14, v20, s1, v23
	v_med3_f32 v15, v15, s1, v23
	v_cvt_pk_fp8_f32 v24, v14, v15 op_sel:[0,0,1]
	v_mul_f32_e32 v15, s5, v47
	v_mul_f32_e32 v20, s5, v43
	v_med3_f32 v15, v15, s1, v23
	v_med3_f32 v20, v20, s1, v23
	v_mov_b32_e32 v29, 0
	v_cvt_pk_fp8_f32 v29, v15, v20
	v_mul_f32_e32 v27, s5, v55
	v_mul_f32_e32 v20, s5, v51
	v_med3_f32 v15, v27, s1, v23
	v_med3_f32 v20, v20, s1, v23
	v_cvt_pk_fp8_f32 v29, v15, v20 op_sel:[0,0,1]
	v_lshl_add_u32 v26, v58, 4, v59
	v_or_b32_e32 v14, v26, v18
	v_lshl_add_u32 v30, v64, 4, v59
	ds_write_b32 v14, v24
	v_or_b32_e32 v14, v30, v18
	ds_write_b32 v14, v29 offset:256
	v_mul_f32_e32 v14, s5, v48
	v_mul_f32_e32 v15, s5, v44
	v_med3_f32 v14, v14, s1, v23
	v_med3_f32 v15, v15, s1, v23
	v_mov_b32_e32 v24, 0
	v_cvt_pk_fp8_f32 v24, v14, v15
	v_mul_f32_e32 v20, s5, v56
	v_mul_f32_e32 v15, s5, v52
	v_med3_f32 v14, v20, s1, v23
	v_med3_f32 v15, v15, s1, v23
	v_cvt_pk_fp8_f32 v24, v14, v15 op_sel:[0,0,1]
	v_mul_f32_e32 v15, s5, v49
	v_mul_f32_e32 v20, s5, v45
	v_med3_f32 v15, v15, s1, v23
	v_med3_f32 v20, v20, s1, v23
	v_mov_b32_e32 v32, 0
	v_cvt_pk_fp8_f32 v32, v15, v20
	v_mul_f32_e32 v27, s5, v57
	v_mul_f32_e32 v20, s5, v53
	v_med3_f32 v15, v27, s1, v23
	v_med3_f32 v20, v20, s1, v23
	v_cvt_pk_fp8_f32 v32, v15, v20 op_sel:[0,0,1]
	v_lshl_add_u32 v29, v62, 4, v59
	v_or_b32_e32 v14, v29, v18
	v_lshl_add_u32 v31, v63, 4, v59
	ds_write_b32 v14, v24 offset:512
	v_or_b32_e32 v14, v31, v18
	s_add_i32 s1, s4, 0x2001
	ds_write_b32 v14, v32 offset:768
	s_cbranch_vccz .LBB0_957
	s_lshr_b32 s12, s4, 4
	s_lshl_b32 s5, s1, 6
	s_lshl_b64 s[18:19], s[12:13], 20
	s_and_b32 s5, s5, 0x340
	s_lshl_b64 s[14:15], s[12:13], 18
	v_lshl_add_u64 v[14:15], v[6:7], 0, s[18:19]
	s_lshl_b32 s12, s5, 2
	v_lshl_add_u64 v[14:15], v[14:15], 0, s[12:13]
	s_add_u32 s12, s42, s14
	s_addc_u32 s13, s43, s15
	s_lshl_b32 s5, s5, 8
	s_add_u32 s14, s12, s5
	v_lshl_add_u64 v[14:15], v[14:15], 0, v[8:9]
	s_addc_u32 s15, s13, 0
	v_and_or_b32 v20, v16, 56, v17
	s_andn2_b64 vcc, exec, s[16:17]
	v_lshlrev_b32_e32 v16, 2, v12
	s_cbranch_vccz .LBB0_958
	s_mov_b32 s1, 0x42800000
	s_mov_b64 s[12:13], 0x100
	s_mov_b64 s[18:19], 0x400
	s_branch .LBB0_959

; __device__ __forceinline__ int otid() { int t = threadIdx.x; asm volatile("" : "+v"(t)); return t; }
; #define CV_MULG(r, g) do { r.x *= g; r.y *= g; r.z *= g; r.w *= g; } while (0)
; __device__ void conv_jobs(const Params& p, unsigned char* smem, int job0, int jstride, int njobs) {
;     const int tid = otid();
;     float4 r0, r1, r2, r3, r4, r5, r6, r7;
;     int job = job0;
;     if (job >= njobs) return;
;     ConvJob cur = conv_job_decode(p, job, tid);
;     CV_LOAD(cur, r0, r1, r2, r3, r4, r5, r6, r7);
;     for (int it = 0;; ++it) {
;         unsigned char* tile = smem + (it & 1) * 16384;
;         if (cur.gain) { const float* g_ = cur.gain; const float g0 = g_[0], g1 = g_[1], g2 = g_[2], g3 = g_[3], g4 = g_[128], g5 = g_[129], g6 = g_[130], g7 = g_[131];
;     ...
;             CV_MULG(r0, g0); CV_MULG(r1, g1); CV_MULG(r2, g2); CV_MULG(r3, g3); CV_MULG(r4, g4); CV_MULG(r5, g5); CV_MULG(r6, g6); CV_MULG(r7, g7);
;     ...
;         }
;         CV_PUT(tile, cur, r0, r1, r2, r3, r4, r5, r6, r7);
;         const int nj = job + jstride;
;         const bool more = nj < njobs;
;         ConvJob nxt = cur;
;         if (more) { nxt = conv_job_decode(p, nj, tid); CV_LOAD(nxt, r0, r1, r2, r3, r4, r5, r6, r7); }
;         __syncthreads();
;         CV_OUT(tile, cur);
;         if (!more) break;
;         cur = nxt; job = nj;
.LBB0_959:
	s_lshl_b32 s16, s18, 2
	s_mov_b32 s17, 0
	global_load_dwordx4 v[32:35], v[14:15], off nt
	v_lshl_add_u64 v[14:15], v[14:15], 0, s[16:17]
	global_load_dwordx4 v[36:39], v[14:15], off nt
	v_lshl_add_u64 v[14:15], v[14:15], 0, s[16:17]
	global_load_dwordx4 v[40:43], v[14:15], off nt
	v_lshl_add_u64 v[14:15], v[14:15], 0, s[16:17]
	global_load_dwordx4 v[44:47], v[14:15], off nt
	s_mulk_i32 s18, 0x1f4
	s_mov_b32 s19, s17
	v_lshl_add_u64 v[14:15], v[14:15], 0, s[18:19]
	global_load_dwordx4 v[48:51], v[14:15], off nt
	v_lshl_add_u64 v[14:15], v[14:15], 0, s[16:17]
	global_load_dwordx4 v[52:55], v[14:15], off nt
	v_lshrrev_b32_e32 v60, 2, v20
	v_lshl_add_u64 v[14:15], v[14:15], 0, s[16:17]
	v_lshrrev_b32_e32 v17, 2, v13
	v_bfe_u32 v27, v13, 5, 1
	v_add_u32_e32 v67, 0x200, v13
	v_add_u32_e32 v24, v21, v18
	v_xor_b32_e32 v21, v60, v12
	v_lshl_add_u64 v[12:13], v[14:15], 0, s[16:17]
	global_load_dwordx4 v[56:59], v[14:15], off nt
	global_load_dwordx4 v[60:63], v[12:13], off nt
	v_and_or_b32 v17, v17, 6, v27
	v_ashrrev_i32_e32 v12, 6, v67
	v_and_or_b32 v14, v12, -8, v17
	v_and_or_b32 v13, v19, -8, v17
	v_xor_b32_e32 v17, v21, v14
	v_lshlrev_b32_e32 v66, 8, v20
	s_mov_b32 s5, 0xc3dc0000
	v_mov_b32_e32 v76, 0x43dc0000
	v_lshlrev_b32_e32 v17, 4, v17
	v_mov_b32_e32 v78, 0
	v_xor_b32_e32 v15, v21, v13
	v_add_u32_e32 v21, v66, v17
	v_mov_b32_e32 v79, 0
	v_mov_b32_e32 v77, 0
	v_lshlrev_b32_e32 v15, 4, v15
	v_mov_b64_e32 v[64:65], s[10:11]
	v_add_u32_e32 v23, v22, v18
	v_add_u32_e32 v22, v66, v15
	v_mad_u64_u32 v[72:73], s[10:11], s0, v20, v[64:65]
	s_waitcnt lgkmcnt(0)
	s_barrier
	ds_read_b128 v[64:67], v22
	ds_read_b128 v[68:71], v21
	v_lshlrev_b32_e32 v12, 4, v13
	v_lshlrev_b32_e32 v14, 4, v14
	v_ashrrev_i32_e32 v13, 31, v12
	v_ashrrev_i32_e32 v15, 31, v14
	v_lshl_add_u64 v[74:75], v[72:73], 0, v[12:13]
	v_add_u32_e32 v28, v28, v18
	v_lshl_add_u64 v[72:73], v[72:73], 0, v[14:15]
	s_waitcnt lgkmcnt(1)
	global_store_dwordx4 v[74:75], v[64:67], off
	s_waitcnt lgkmcnt(0)
	global_store_dwordx4 v[72:73], v[68:71], off
	v_mov_b32_e32 v9, 0
	v_add_u32_e32 v29, v29, v18
	s_andn2_b64 vcc, exec, s[8:9]
	s_waitcnt vmcnt(9)
	v_mul_f32_e32 v19, s1, v33
	v_mul_f32_e32 v27, s1, v34
	s_waitcnt vmcnt(8)
	v_mul_f32_e32 v34, s1, v37
	v_mul_f32_e32 v17, s1, v32
	v_mul_f32_e32 v32, s1, v35
	v_med3_f32 v19, v19, s5, v76
	v_mul_f32_e32 v35, s1, v38
	v_med3_f32 v34, v34, s5, v76
	v_med3_f32 v27, v27, s5, v76
	v_mul_f32_e32 v33, s1, v36
	v_med3_f32 v35, v35, s5, v76
	v_cvt_pk_fp8_f32 v78, v19, v34
	v_med3_f32 v17, v17, s5, v76
	v_med3_f32 v33, v33, s5, v76
	v_cvt_pk_fp8_f32 v79, v27, v35
	s_waitcnt vmcnt(7)
	v_mul_f32_e32 v37, s1, v41
	v_cvt_pk_fp8_f32 v77, v17, v33
	s_waitcnt vmcnt(6)
	v_mul_f32_e32 v33, s1, v45
	v_mul_f32_e32 v38, s1, v42
	v_med3_f32 v17, v37, s5, v76
	v_mul_f32_e32 v34, s1, v46
	v_med3_f32 v33, v33, s5, v76
	v_med3_f32 v19, v38, s5, v76
	v_cvt_pk_fp8_f32 v78, v17, v33 op_sel:[0,0,1]
	v_med3_f32 v17, v34, s5, v76
	v_cvt_pk_fp8_f32 v79, v19, v17 op_sel:[0,0,1]
	v_mul_f32_e32 v17, s1, v39
	v_med3_f32 v32, v32, s5, v76
	v_med3_f32 v17, v17, s5, v76
	v_mov_b32_e32 v33, 0
	v_cvt_pk_fp8_f32 v33, v32, v17
	v_mul_f32_e32 v19, s1, v43
	v_med3_f32 v17, v19, s5, v76
	v_mul_f32_e32 v19, s1, v47
	v_med3_f32 v19, v19, s5, v76
	v_cvt_pk_fp8_f32 v33, v17, v19 op_sel:[0,0,1]
	s_waitcnt vmcnt(5)
	v_mul_f32_e32 v17, s1, v48
	s_waitcnt vmcnt(4)
	v_mul_f32_e32 v19, s1, v52
	v_mul_f32_e32 v36, s1, v40
	v_mul_f32_e32 v40, s1, v44
	v_med3_f32 v17, v17, s5, v76
	v_med3_f32 v19, v19, s5, v76
	v_mov_b32_e32 v32, 0
	v_med3_f32 v36, v36, s5, v76
	v_med3_f32 v27, v40, s5, v76
	v_cvt_pk_fp8_f32 v32, v17, v19
	v_cvt_pk_fp8_f32 v77, v36, v27 op_sel:[0,0,1]
	v_add_u32_e32 v27, v25, v18
	s_waitcnt vmcnt(3)
	v_mul_f32_e32 v25, s1, v56
	s_waitcnt vmcnt(2)
	v_mul_f32_e32 v19, s1, v60
	v_med3_f32 v17, v25, s5, v76
	v_med3_f32 v19, v19, s5, v76
	v_cvt_pk_fp8_f32 v32, v17, v19 op_sel:[0,0,1]
	v_mul_f32_e32 v17, s1, v49
	v_mul_f32_e32 v19, s1, v53
	ds_write_b32 v23, v77 offset:16384
	ds_write_b32 v24, v78 offset:16640
	ds_write_b32 v27, v79 offset:16896
	ds_write_b32 v28, v33 offset:17152
	v_med3_f32 v17, v17, s5, v76
	v_med3_f32 v19, v19, s5, v76
	v_mov_b32_e32 v33, 0
	v_cvt_pk_fp8_f32 v33, v17, v19
	v_mul_f32_e32 v25, s1, v57
	v_mul_f32_e32 v19, s1, v61
	v_med3_f32 v17, v25, s5, v76
	v_med3_f32 v19, v19, s5, v76
	v_cvt_pk_fp8_f32 v33, v17, v19 op_sel:[0,0,1]
	v_add_u32_e32 v25, v26, v18
	v_mul_f32_e32 v17, s1, v50
	v_mul_f32_e32 v19, s1, v54
	ds_write_b32 v25, v32 offset:16384
	v_med3_f32 v17, v17, s5, v76
	v_med3_f32 v19, v19, s5, v76
	v_mov_b32_e32 v32, 0
	v_cvt_pk_fp8_f32 v32, v17, v19
	v_add_u32_e32 v26, v30, v18
	v_mul_f32_e32 v30, s1, v58
	v_mul_f32_e32 v19, s1, v62
	v_med3_f32 v17, v30, s5, v76
	v_med3_f32 v19, v19, s5, v76
	v_cvt_pk_fp8_f32 v32, v17, v19 op_sel:[0,0,1]
	v_mul_f32_e32 v17, s1, v51
	v_mul_f32_e32 v19, s1, v55
	ds_write_b32 v26, v33 offset:16640
	v_med3_f32 v17, v17, s5, v76
	v_med3_f32 v19, v19, s5, v76
	v_mov_b32_e32 v33, 0
	v_cvt_pk_fp8_f32 v33, v17, v19
	v_mul_f32_e32 v30, s1, v59
	v_mul_f32_e32 v19, s1, v63
	v_med3_f32 v17, v30, s5, v76
	v_med3_f32 v19, v19, s5, v76
	v_cvt_pk_fp8_f32 v33, v17, v19 op_sel:[0,0,1]
	v_cndmask_b32_e64 v17, 0, 1, s[8:9]
	v_add_u32_e32 v30, v31, v18
	v_cmp_ne_u32_e64 s[0:1], 1, v17
	s_add_i32 s5, s4, 0x2002
	ds_write_b32 v29, v32 offset:16896
	ds_write_b32 v30, v33 offset:17152
	s_cbranch_vccnz .LBB0_962
	s_lshr_b32 s16, s4, 4
	s_lshl_b64 s[10:11], s[16:17], 20
	v_lshl_add_u64 v[18:19], v[6:7], 0, s[10:11]
	s_lshl_b32 s10, s5, 6
	s_and_b32 s10, s10, 0x380
	s_lshl_b64 s[8:9], s[16:17], 18
	s_lshl_b32 s16, s10, 2
	s_add_u32 s8, s42, s8
	s_addc_u32 s9, s43, s9
	s_lshl_b32 s10, s10, 8
	v_lshl_add_u64 v[18:19], v[18:19], 0, s[16:17]
	s_add_u32 s10, s8, s10
	v_lshl_add_u64 v[18:19], v[18:19], 0, v[8:9]
	s_addc_u32 s11, s9, 0
	s_cbranch_execz .LBB0_963
	s_mov_b32 s5, 0x42800000
	s_mov_b64 s[8:9], 0x100
	s_mov_b64 s[18:19], 0x400
	s_branch .LBB0_964

; __device__ __forceinline__ int otid() { int t = threadIdx.x; asm volatile("" : "+v"(t)); return t; }
; #define CV_MULG(r, g) do { r.x *= g; r.y *= g; r.z *= g; r.w *= g; } while (0)
; __device__ void conv_jobs(const Params& p, unsigned char* smem, int job0, int jstride, int njobs) {
;     const int tid = otid();
;     float4 r0, r1, r2, r3, r4, r5, r6, r7;
;     int job = job0;
;     if (job >= njobs) return;
;     ConvJob cur = conv_job_decode(p, job, tid);
;     CV_LOAD(cur, r0, r1, r2, r3, r4, r5, r6, r7);
;     for (int it = 0;; ++it) {
;         unsigned char* tile = smem + (it & 1) * 16384;
;         if (cur.gain) { const float* g_ = cur.gain; const float g0 = g_[0], g1 = g_[1], g2 = g_[2], g3 = g_[3], g4 = g_[128], g5 = g_[129], g6 = g_[130], g7 = g_[131];
;     ...
;             CV_MULG(r0, g0); CV_MULG(r1, g1); CV_MULG(r2, g2); CV_MULG(r3, g3); CV_MULG(r4, g4); CV_MULG(r5, g5); CV_MULG(r6, g6); CV_MULG(r7, g7);
;     ...
;         }
;         CV_PUT(tile, cur, r0, r1, r2, r3, r4, r5, r6, r7);
;         const int nj = job + jstride;
;         const bool more = nj < njobs;
;         ConvJob nxt = cur;
;         if (more) { nxt = conv_job_decode(p, nj, tid); CV_LOAD(nxt, r0, r1, r2, r3, r4, r5, r6, r7); }
;         __syncthreads();
;         CV_OUT(tile, cur);
;         if (!more) break;
;         cur = nxt; job = nj;
.LBB0_964:
	s_lshl_b32 s16, s18, 2
	global_load_dwordx4 v[32:35], v[18:19], off nt
	v_lshl_add_u64 v[18:19], v[18:19], 0, s[16:17]
	global_load_dwordx4 v[36:39], v[18:19], off nt
	v_lshl_add_u64 v[18:19], v[18:19], 0, s[16:17]
	global_load_dwordx4 v[40:43], v[18:19], off nt
	v_lshl_add_u64 v[18:19], v[18:19], 0, s[16:17]
	s_mulk_i32 s18, 0x1f4
	s_mov_b32 s19, s17
	global_load_dwordx4 v[44:47], v[18:19], off nt
	v_lshl_add_u64 v[18:19], v[18:19], 0, s[18:19]
	global_load_dwordx4 v[48:51], v[18:19], off nt
	v_lshl_add_u64 v[18:19], v[18:19], 0, s[16:17]
	global_load_dwordx4 v[52:55], v[18:19], off nt
	v_lshl_add_u64 v[18:19], v[18:19], 0, s[16:17]
	global_load_dwordx4 v[56:59], v[18:19], off nt
	v_lshl_add_u64 v[18:19], v[18:19], 0, s[16:17]
	global_load_dwordx4 v[60:63], v[18:19], off nt
	s_waitcnt lgkmcnt(0)
	s_barrier
	ds_read_b128 v[64:67], v22 offset:16384
	ds_read_b128 v[68:71], v21 offset:16384
	v_mov_b64_e32 v[18:19], s[14:15]
	v_mad_u64_u32 v[18:19], s[12:13], s12, v20, v[18:19]
	v_lshl_add_u64 v[72:73], v[18:19], 0, v[12:13]
	v_lshl_add_u64 v[18:19], v[18:19], 0, v[14:15]
	s_mov_b32 s9, 0xc3dc0000
	v_mov_b32_e32 v17, 0x43dc0000
	s_waitcnt lgkmcnt(1)
	global_store_dwordx4 v[72:73], v[64:67], off
	s_waitcnt lgkmcnt(0)
	global_store_dwordx4 v[18:19], v[68:71], off
	v_mov_b32_e32 v31, 0
	v_mov_b32_e32 v75, 0
	v_mov_b32_e32 v76, 0
	v_mov_b32_e32 v74, 0
	v_mov_b32_e32 v77, 0
	v_mov_b32_e32 v9, 0
	s_and_b64 vcc, exec, s[0:1]
	s_waitcnt vmcnt(9)
	v_mul_f32_e32 v18, s5, v32
	v_mul_f32_e32 v19, s5, v33
	v_mul_f32_e32 v32, s5, v34
	v_mul_f32_e32 v33, s5, v35
	s_waitcnt vmcnt(8)
	v_mul_f32_e32 v34, s5, v36
	v_mul_f32_e32 v35, s5, v37
	v_mul_f32_e32 v36, s5, v38
	v_mul_f32_e32 v37, s5, v39
	v_med3_f32 v18, v18, s9, v17
	v_med3_f32 v32, v32, s9, v17
	v_med3_f32 v33, v33, s9, v17
	v_med3_f32 v34, v34, s9, v17
	s_waitcnt vmcnt(7)
	v_mul_f32_e32 v39, s5, v41
	v_med3_f32 v36, v36, s9, v17
	v_med3_f32 v37, v37, s9, v17
	v_med3_f32 v19, v19, s9, v17
	v_med3_f32 v35, v35, s9, v17
	v_cvt_pk_fp8_f32 v31, v18, v34
	v_med3_f32 v18, v39, s9, v17
	v_cvt_pk_fp8_f32 v75, v32, v36
	v_cvt_pk_fp8_f32 v76, v33, v37
	s_waitcnt vmcnt(5)
	v_mul_f32_e32 v37, s5, v48
	s_waitcnt vmcnt(4)
	v_mul_f32_e32 v39, s5, v52
	v_cvt_pk_fp8_f32 v74, v19, v35
	v_med3_f32 v37, v37, s9, v17
	v_med3_f32 v39, v39, s9, v17
	v_mul_f32_e32 v38, s5, v40
	v_mul_f32_e32 v40, s5, v42
	v_mul_f32_e32 v35, s5, v46
	v_cvt_pk_fp8_f32 v77, v37, v39
	v_mul_f32_e32 v34, s5, v45
	v_med3_f32 v19, v40, s9, v17
	v_med3_f32 v35, v35, s9, v17
	v_mul_f32_e32 v42, s5, v44
	v_med3_f32 v34, v34, s9, v17
	s_waitcnt vmcnt(3)
	v_mul_f32_e32 v40, s5, v56
	v_cvt_pk_fp8_f32 v75, v19, v35 op_sel:[0,0,1]
	s_waitcnt vmcnt(2)
	v_mul_f32_e32 v19, s5, v60
	v_mul_f32_e32 v41, s5, v43
	v_med3_f32 v38, v38, s9, v17
	v_mul_f32_e32 v36, s5, v47
	v_med3_f32 v33, v42, s9, v17
	v_cvt_pk_fp8_f32 v74, v18, v34 op_sel:[0,0,1]
	v_med3_f32 v18, v40, s9, v17
	v_med3_f32 v19, v19, s9, v17
	v_med3_f32 v32, v41, s9, v17
	v_med3_f32 v36, v36, s9, v17
	v_cvt_pk_fp8_f32 v31, v38, v33 op_sel:[0,0,1]
	v_cvt_pk_fp8_f32 v77, v18, v19 op_sel:[0,0,1]
	v_mul_f32_e32 v18, s5, v49
	v_mul_f32_e32 v19, s5, v53
	v_cvt_pk_fp8_f32 v76, v32, v36 op_sel:[0,0,1]
	v_med3_f32 v18, v18, s9, v17
	v_med3_f32 v19, v19, s9, v17
	v_mov_b32_e32 v32, 0
	v_cvt_pk_fp8_f32 v32, v18, v19
	ds_write_b32 v23, v31
	ds_write_b32 v24, v74 offset:256
	ds_write_b32 v27, v75 offset:512
	ds_write_b32 v28, v76 offset:768
	v_mul_f32_e32 v31, s5, v57
	v_mul_f32_e32 v19, s5, v61
	v_med3_f32 v18, v31, s9, v17
	v_med3_f32 v19, v19, s9, v17
	v_cvt_pk_fp8_f32 v32, v18, v19 op_sel:[0,0,1]
	v_mul_f32_e32 v18, s5, v50
	v_mul_f32_e32 v19, s5, v54
	v_med3_f32 v18, v18, s9, v17
	v_med3_f32 v19, v19, s9, v17
	v_mov_b32_e32 v33, 0
	v_cvt_pk_fp8_f32 v33, v18, v19
	v_mul_f32_e32 v31, s5, v58
	v_mul_f32_e32 v19, s5, v62
	v_med3_f32 v18, v31, s9, v17
	v_med3_f32 v19, v19, s9, v17
	v_cvt_pk_fp8_f32 v33, v18, v19 op_sel:[0,0,1]
	v_mul_f32_e32 v18, s5, v51
	v_mul_f32_e32 v19, s5, v55
	v_med3_f32 v18, v18, s9, v17
	v_med3_f32 v19, v19, s9, v17
	v_mov_b32_e32 v34, 0
	v_cvt_pk_fp8_f32 v34, v18, v19
	v_mul_f32_e32 v31, s5, v59
	v_mul_f32_e32 v19, s5, v63
	v_med3_f32 v18, v31, s9, v17
	v_med3_f32 v17, v19, s9, v17
	v_cvt_pk_fp8_f32 v34, v18, v17 op_sel:[0,0,1]
	s_add_i32 s5, s4, 0x2003
	ds_write_b32 v25, v77
	ds_write_b32 v26, v32 offset:256
	ds_write_b32 v29, v33 offset:512
	ds_write_b32 v30, v34 offset:768
	s_cbranch_vccnz .LBB0_967
	s_lshr_b32 s16, s4, 4
	s_lshl_b32 s4, s5, 6
	s_and_b32 s4, s4, 0x3c0
	s_lshl_b64 s[0:1], s[16:17], 18
	s_lshl_b64 s[12:13], s[16:17], 20
	s_lshl_b32 s16, s4, 2
	s_add_u32 s0, s42, s0
	v_lshl_add_u64 v[6:7], v[6:7], 0, s[12:13]
	s_addc_u32 s1, s43, s1
	s_lshl_b32 s4, s4, 8
	v_lshl_add_u64 v[6:7], v[6:7], 0, s[16:17]
	s_add_u32 s0, s0, s4
	v_lshl_add_u64 v[6:7], v[6:7], 0, v[8:9]
	s_addc_u32 s1, s1, 0
	s_cbranch_execz .LBB0_968
	s_mov_b32 s4, 0x42800000
	s_mov_b64 s[12:13], 0x100
	s_mov_b64 s[14:15], 0x400
	s_branch .LBB0_969

; __device__ __forceinline__ int otid() { int t = threadIdx.x; asm volatile("" : "+v"(t)); return t; }
; #define CV_MULG(r, g) do { r.x *= g; r.y *= g; r.z *= g; r.w *= g; } while (0)
; __device__ void conv_jobs(const Params& p, unsigned char* smem, int job0, int jstride, int njobs) {
;     const int tid = otid();
;     float4 r0, r1, r2, r3, r4, r5, r6, r7;
;     int job = job0;
;     if (job >= njobs) return;
;     ConvJob cur = conv_job_decode(p, job, tid);
;     CV_LOAD(cur, r0, r1, r2, r3, r4, r5, r6, r7);
;     for (int it = 0;; ++it) {
;         unsigned char* tile = smem + (it & 1) * 16384;
;         if (cur.gain) { const float* g_ = cur.gain; const float g0 = g_[0], g1 = g_[1], g2 = g_[2], g3 = g_[3], g4 = g_[128], g5 = g_[129], g6 = g_[130], g7 = g_[131];
;     ...
;             CV_MULG(r0, g0); CV_MULG(r1, g1); CV_MULG(r2, g2); CV_MULG(r3, g3); CV_MULG(r4, g4); CV_MULG(r5, g5); CV_MULG(r6, g6); CV_MULG(r7, g7);
;     ...
;         }
;         CV_PUT(tile, cur, r0, r1, r2, r3, r4, r5, r6, r7);
;         const int nj = job + jstride;
;         const bool more = nj < njobs;
;         ConvJob nxt = cur;
;         if (more) { nxt = conv_job_decode(p, nj, tid); CV_LOAD(nxt, r0, r1, r2, r3, r4, r5, r6, r7); }
;         __syncthreads();
;         CV_OUT(tile, cur);
;         if (!more) break;
;         cur = nxt; job = nj;
;     }
;     __syncthreads();
; __device__ void phase5a(const Params& p, unsigned char* smem, unsigned* rsync) {
;     ...
;     for (;;) {
;         __syncthreads();
;         if (threadIdx.x == 0) *qslot = (int)__hip_atomic_fetch_add(qctr, 1u, __ATOMIC_RELAXED, __HIP_MEMORY_SCOPE_AGENT);
.LBB0_969:
	s_lshl_b32 s16, s14, 2
	v_lshl_add_u64 v[10:11], v[6:7], 0, s[16:17]
	global_load_dwordx4 v[2:5], v[6:7], off nt
	s_mulk_i32 s14, 0x1f4
	global_load_dwordx4 v[6:9], v[10:11], off nt
	v_lshl_add_u64 v[10:11], v[10:11], 0, s[16:17]
	global_load_dwordx4 v[16:19], v[10:11], off nt
	v_lshl_add_u64 v[10:11], v[10:11], 0, s[16:17]
	s_mov_b32 s15, s17
	global_load_dwordx4 v[32:35], v[10:11], off nt
	v_lshl_add_u64 v[10:11], v[10:11], 0, s[14:15]
	global_load_dwordx4 v[36:39], v[10:11], off nt
	v_lshl_add_u64 v[10:11], v[10:11], 0, s[16:17]
	global_load_dwordx4 v[40:43], v[10:11], off nt
	v_lshl_add_u64 v[10:11], v[10:11], 0, s[16:17]
	global_load_dwordx4 v[44:47], v[10:11], off nt
	v_lshl_add_u64 v[10:11], v[10:11], 0, s[16:17]
	global_load_dwordx4 v[48:51], v[10:11], off nt
	s_waitcnt lgkmcnt(0)
	s_barrier
	ds_read_b128 v[52:55], v22
	ds_read_b128 v[56:59], v21
	v_mov_b64_e32 v[10:11], s[10:11]
	v_mad_u64_u32 v[10:11], s[8:9], s8, v20, v[10:11]
	s_mov_b32 s5, 0xc3dc0000
	v_mov_b32_e32 v31, 0x43dc0000
	v_lshl_add_u64 v[60:61], v[10:11], 0, v[12:13]
	v_lshl_add_u64 v[10:11], v[10:11], 0, v[14:15]
	v_mov_b32_e32 v63, 0
	v_mov_b32_e32 v65, 0
	v_mov_b32_e32 v66, 0
	s_waitcnt lgkmcnt(1)
	global_store_dwordx4 v[60:61], v[52:55], off
	s_waitcnt lgkmcnt(0)
	global_store_dwordx4 v[10:11], v[56:59], off
	v_mov_b32_e32 v64, 0
	v_mov_b32_e32 v67, 0
	v_mov_b32_e32 v62, 0
	s_waitcnt vmcnt(9)
	v_mul_f32_e32 v2, s4, v2
	v_mul_f32_e32 v4, s4, v4
	v_mul_f32_e32 v5, s4, v5
	s_waitcnt vmcnt(8)
	v_mul_f32_e32 v6, s4, v6
	v_mul_f32_e32 v8, s4, v8
	v_mul_f32_e32 v9, s4, v9
	v_mul_f32_e32 v3, s4, v3
	v_med3_f32 v2, v2, s5, v31
	v_med3_f32 v4, v4, s5, v31
	v_med3_f32 v5, v5, s5, v31
	v_mul_f32_e32 v7, s4, v7
	v_med3_f32 v6, v6, s5, v31
	s_waitcnt vmcnt(7)
	v_mul_f32_e32 v11, s4, v17
	v_med3_f32 v8, v8, s5, v31
	v_med3_f32 v9, v9, s5, v31
	v_med3_f32 v3, v3, s5, v31
	v_med3_f32 v7, v7, s5, v31
	v_cvt_pk_fp8_f32 v63, v2, v6
	v_med3_f32 v2, v11, s5, v31
	v_cvt_pk_fp8_f32 v65, v4, v8
	v_cvt_pk_fp8_f32 v66, v5, v9
	s_waitcnt vmcnt(5)
	v_mul_f32_e32 v9, s4, v36
	s_waitcnt vmcnt(4)
	v_mul_f32_e32 v11, s4, v40
	v_cvt_pk_fp8_f32 v64, v3, v7
	v_med3_f32 v9, v9, s5, v31
	v_med3_f32 v11, v11, s5, v31
	v_mul_f32_e32 v10, s4, v16
	v_mul_f32_e32 v16, s4, v18
	v_mul_f32_e32 v7, s4, v34
	v_cvt_pk_fp8_f32 v67, v9, v11
	v_mul_f32_e32 v6, s4, v33
	v_med3_f32 v3, v16, s5, v31
	v_med3_f32 v7, v7, s5, v31
	v_med3_f32 v6, v6, s5, v31
	s_waitcnt vmcnt(3)
	v_mul_f32_e32 v16, s4, v44
	v_cvt_pk_fp8_f32 v65, v3, v7 op_sel:[0,0,1]
	s_waitcnt vmcnt(2)
	v_mul_f32_e32 v3, s4, v48
	v_mul_f32_e32 v18, s4, v32
	v_cvt_pk_fp8_f32 v64, v2, v6 op_sel:[0,0,1]
	v_med3_f32 v2, v16, s5, v31
	v_med3_f32 v3, v3, s5, v31
	v_med3_f32 v10, v10, s5, v31
	v_med3_f32 v5, v18, s5, v31
	v_cvt_pk_fp8_f32 v67, v2, v3 op_sel:[0,0,1]
	v_mul_f32_e32 v2, s4, v37
	v_mul_f32_e32 v3, s4, v41
	v_cvt_pk_fp8_f32 v63, v10, v5 op_sel:[0,0,1]
	v_med3_f32 v2, v2, s5, v31
	v_med3_f32 v3, v3, s5, v31
	v_mov_b32_e32 v5, 0
	v_mul_f32_e32 v17, s4, v19
	v_mul_f32_e32 v8, s4, v35
	v_cvt_pk_fp8_f32 v5, v2, v3
	v_med3_f32 v4, v17, s5, v31
	v_med3_f32 v8, v8, s5, v31
	v_cvt_pk_fp8_f32 v66, v4, v8 op_sel:[0,0,1]
	v_mul_f32_e32 v4, s4, v45
	v_mul_f32_e32 v3, s4, v49
	v_med3_f32 v2, v4, s5, v31
	v_med3_f32 v3, v3, s5, v31
	v_cvt_pk_fp8_f32 v5, v2, v3 op_sel:[0,0,1]
	v_mul_f32_e32 v2, s4, v38
	v_mul_f32_e32 v3, s4, v42
	v_med3_f32 v2, v2, s5, v31
	v_med3_f32 v3, v3, s5, v31
	v_mov_b32_e32 v6, 0
	v_cvt_pk_fp8_f32 v6, v2, v3
	v_mul_f32_e32 v4, s4, v46
	v_mul_f32_e32 v3, s4, v50
	v_med3_f32 v2, v4, s5, v31
	v_med3_f32 v3, v3, s5, v31
	v_cvt_pk_fp8_f32 v6, v2, v3 op_sel:[0,0,1]
	v_mul_f32_e32 v2, s4, v39
	v_mul_f32_e32 v3, s4, v43
	v_med3_f32 v2, v2, s5, v31
	v_med3_f32 v3, v3, s5, v31
	v_cvt_pk_fp8_f32 v62, v2, v3
	v_mul_f32_e32 v4, s4, v47
	v_mul_f32_e32 v3, s4, v51
	v_med3_f32 v2, v4, s5, v31
	v_med3_f32 v3, v3, s5, v31
	v_cvt_pk_fp8_f32 v62, v2, v3 op_sel:[0,0,1]
	ds_write_b32 v23, v63 offset:16384
	ds_write_b32 v24, v64 offset:16640
	ds_write_b32 v27, v65 offset:16896
	ds_write_b32 v28, v66 offset:17152
	ds_write_b32 v25, v67 offset:16384
	ds_write_b32 v26, v5 offset:16640
	ds_write_b32 v29, v6 offset:16896
	ds_write_b32 v30, v62 offset:17152
	s_waitcnt lgkmcnt(0)
	s_barrier
	ds_read_b128 v[2:5], v22 offset:16384
	ds_read_b128 v[6:9], v21 offset:16384
	v_mov_b64_e32 v[10:11], s[0:1]
	v_mad_u64_u32 v[10:11], s[0:1], s12, v20, v[10:11]
	v_lshl_add_u64 v[12:13], v[10:11], 0, v[12:13]
	s_waitcnt lgkmcnt(1)
	global_store_dwordx4 v[12:13], v[2:5], off
	s_nop 1
	v_lshl_add_u64 v[2:3], v[10:11], 0, v[14:15]
	s_waitcnt lgkmcnt(0)
	global_store_dwordx4 v[2:3], v[6:9], off
	s_barrier
	s_barrier
	s_and_saveexec_b64 s[0:1], s[72:73]
	s_cbranch_execz .LBB0_973
	s_mov_b64 s[10:11], exec
	v_mbcnt_lo_u32_b32 v2, s10, 0
	v_mbcnt_hi_u32_b32 v2, s11, v2
	v_cmp_eq_u32_e32 vcc, 0, v2
	s_and_saveexec_b64 s[8:9], vcc
	s_cbranch_execz .LBB0_972
	s_bcnt1_i32_b64 s4, s[10:11]
	v_mov_b32_e32 v3, 0
	v_mov_b32_e32 v4, s4
	global_atomic_add v3, v3, v4, s[6:7] sc0

; __device__ __forceinline__ ConvJob conv_job_decode(const Params& p, int job, int tid) {
;     ...
;         const int q = job - 8192, e = q >> 4, ng = q & 15;
;         j.sp = p.we_down + (size_t)e * 262144 + (size_t)kr * 1024 + ng * 64 + n4; j.ldsrc = 1024;
;         j.dst8 = p.dT8 + (size_t)e * 262144 + (size_t)(ng * 64) * 256; j.ld8 = 256; j.s8 = D8S;
.LBB0_979:
	s_lshl_b32 s1, s14, 2
	s_mul_i32 s12, s14, 0x20c
	s_mov_b32 s13, 0
	s_sub_u32 s16, 0, s1
	v_lshl_add_u64 v[14:15], v[10:11], 0, s[12:13]
	s_subb_u32 s17, 0, 0
	v_lshl_add_u64 v[20:21], v[14:15], 0, s[16:17]
	v_lshl_add_u64 v[22:23], v[20:21], 0, s[16:17]
	v_lshl_add_u64 v[24:25], v[22:23], 0, s[16:17]
	v_mov_b32_e32 v9, 0xfffffe0c
	v_mad_i64_i32 v[16:17], s[14:15], s14, v9, v[24:25]
	global_load_dwordx4 v[26:29], v[16:17], off nt
	v_lshl_add_u64 v[16:17], v[16:17], 0, s[16:17]
	global_load_dwordx4 v[30:33], v[16:17], off nt
	v_lshl_add_u64 v[16:17], v[16:17], 0, s[16:17]
	global_load_dwordx4 v[34:37], v[10:11], off nt
	global_load_dwordx4 v[38:41], v[16:17], off nt
	global_load_dwordx4 v[42:45], v[22:23], off nt
	global_load_dwordx4 v[46:49], v[24:25], off nt
	global_load_dwordx4 v[50:53], v[14:15], off nt
	global_load_dwordx4 v[54:57], v[20:21], off nt
	s_mov_b32 s1, 0xc3dc0000
	v_mov_b32_e32 v23, 0x43dc0000
	v_mov_b32_e32 v14, 0
	v_mov_b32_e32 v15, 0
	v_ashrrev_i32_e32 v10, 4, v13
	v_lshrrev_b32_e32 v58, 2, v8
	v_ashrrev_i32_e32 v19, 6, v13
	v_lshlrev_b32_e32 v59, 8, v8
	v_mov_b32_e32 v11, s47
	v_mov_b32_e32 v18, s45
	v_add_u32_e32 v21, 32, v10
	v_xor_b32_e32 v22, v58, v19
	v_lshlrev_b32_e32 v24, 2, v10
	v_xor_b32_e32 v25, 4, v58
	v_cmp_gt_u32_e32 vcc, 32, v8
	v_mov_b32_e32 v60, s46
	v_mov_b32_e32 v61, s44
	v_xor_b32_e32 v62, 8, v58
	v_xor_b32_e32 v63, 12, v58
	v_cndmask_b32_e32 v11, v11, v18, vcc
	v_and_b32_e32 v18, 12, v24
	v_xor_b32_e32 v24, v25, v19
	v_ashrrev_i32_e32 v21, 2, v21
	v_lshl_add_u32 v22, v22, 4, v59
	v_cndmask_b32_e32 v10, v60, v61, vcc
	v_xor_b32_e32 v60, v62, v19
	v_xor_b32_e32 v61, v63, v19
	v_xor_b32_e32 v58, v21, v58
	v_xor_b32_e32 v64, v25, v21
	v_xor_b32_e32 v62, v62, v21
	v_xor_b32_e32 v63, v63, v21
	v_or_b32_e32 v65, v22, v18
	v_lshl_add_u32 v21, v24, 4, v59
	v_mov_b32_e32 v20, 0
	v_or_b32_e32 v24, v21, v18
	v_lshl_add_u32 v25, v60, 4, v59
	v_or_b32_e32 v60, v25, v18
	v_lshrrev_b32_e32 v16, 3, v13
	v_and_b32_e32 v17, 7, v13
	v_lshl_add_u64 v[6:7], s[48:49], 0, v[6:7]
	s_mov_b64 s[16:17], 0
	v_mov_b32_e32 v9, 0
	s_and_b64 vcc, exec, s[8:9]
	v_lshlrev_b32_e32 v8, 2, v8
	s_waitcnt vmcnt(7)
	v_mul_f32_e32 v26, s5, v26
	v_mul_f32_e32 v27, s5, v27
	s_waitcnt vmcnt(6)
	v_mul_f32_e32 v30, s5, v30
	s_waitcnt vmcnt(5)
	v_mul_f32_e32 v34, s5, v34
	s_waitcnt vmcnt(4)
	v_mul_f32_e32 v38, s5, v38
	v_mul_f32_e32 v35, s5, v35
	v_mul_f32_e32 v39, s5, v39
	v_med3_f32 v34, v34, s1, v23
	v_med3_f32 v38, v38, s1, v23
	v_med3_f32 v35, v35, s1, v23
	v_med3_f32 v39, v39, s1, v23
	v_cvt_pk_fp8_f32 v14, v34, v38
	v_cvt_pk_fp8_f32 v15, v35, v39
	v_med3_f32 v26, v26, s1, v23
	v_mul_f32_e32 v31, s5, v31
	v_med3_f32 v30, v30, s1, v23
	v_med3_f32 v27, v27, s1, v23
	v_med3_f32 v31, v31, s1, v23
	v_cvt_pk_fp8_f32 v14, v30, v26 op_sel:[0,0,1]
	v_cvt_pk_fp8_f32 v15, v31, v27 op_sel:[0,0,1]
	v_mul_f32_e32 v36, s5, v36
	v_mul_f32_e32 v40, s5, v40
	v_mul_f32_e32 v37, s5, v37
	v_mul_f32_e32 v41, s5, v41
	v_med3_f32 v36, v36, s1, v23
	v_med3_f32 v40, v40, s1, v23
	v_med3_f32 v34, v37, s1, v23
	v_med3_f32 v26, v41, s1, v23
	ds_write_b32 v65, v14
	ds_write_b32 v24, v15 offset:256
	v_mov_b32_e32 v15, 0
	v_cvt_pk_fp8_f32 v20, v36, v40
	v_cvt_pk_fp8_f32 v15, v34, v26
	v_mul_f32_e32 v28, s5, v28
	v_mul_f32_e32 v32, s5, v32
	v_mul_f32_e32 v14, s5, v33
	v_mul_f32_e32 v24, s5, v29
	v_med3_f32 v28, v28, s1, v23
	v_med3_f32 v32, v32, s1, v23
	v_med3_f32 v14, v14, s1, v23
	v_med3_f32 v24, v24, s1, v23
	v_cvt_pk_fp8_f32 v20, v32, v28 op_sel:[0,0,1]
	v_cvt_pk_fp8_f32 v15, v14, v24 op_sel:[0,0,1]
	v_lshl_add_u32 v28, v61, 4, v59
	v_or_b32_e32 v14, v28, v18
	ds_write_b32 v60, v20 offset:512
	ds_write_b32 v14, v15 offset:768
	s_waitcnt vmcnt(2)
	v_mul_f32_e32 v14, s5, v46
	v_mul_f32_e32 v15, s5, v42
	v_med3_f32 v14, v14, s1, v23
	v_med3_f32 v15, v15, s1, v23
	v_mov_b32_e32 v24, 0
	v_cvt_pk_fp8_f32 v24, v14, v15
	s_waitcnt vmcnt(0)
	v_mul_f32_e32 v20, s5, v54
	v_mul_f32_e32 v15, s5, v50
	v_med3_f32 v14, v20, s1, v23
	v_med3_f32 v15, v15, s1, v23
	v_cvt_pk_fp8_f32 v24, v14, v15 op_sel:[0,0,1]
	v_mul_f32_e32 v15, s5, v47
	v_mul_f32_e32 v20, s5, v43
	v_med3_f32 v15, v15, s1, v23
	v_med3_f32 v20, v20, s1, v23
	v_mov_b32_e32 v29, 0
	v_cvt_pk_fp8_f32 v29, v15, v20
	v_mul_f32_e32 v27, s5, v55
	v_mul_f32_e32 v20, s5, v51
	v_med3_f32 v15, v27, s1, v23
	v_med3_f32 v20, v20, s1, v23
	v_cvt_pk_fp8_f32 v29, v15, v20 op_sel:[0,0,1]
	v_lshl_add_u32 v26, v58, 4, v59
	v_or_b32_e32 v14, v26, v18
	v_lshl_add_u32 v30, v64, 4, v59
	ds_write_b32 v14, v24
	v_or_b32_e32 v14, v30, v18
	ds_write_b32 v14, v29 offset:256
	v_mul_f32_e32 v14, s5, v48
	v_mul_f32_e32 v15, s5, v44
	v_med3_f32 v14, v14, s1, v23
	v_med3_f32 v15, v15, s1, v23
	v_mov_b32_e32 v24, 0
	v_cvt_pk_fp8_f32 v24, v14, v15
	v_mul_f32_e32 v20, s5, v56
	v_mul_f32_e32 v15, s5, v52
	v_med3_f32 v14, v20, s1, v23
	v_med3_f32 v15, v15, s1, v23
	v_cvt_pk_fp8_f32 v24, v14, v15 op_sel:[0,0,1]
	v_mul_f32_e32 v15, s5, v49
	v_mul_f32_e32 v20, s5, v45
	v_med3_f32 v15, v15, s1, v23
	v_med3_f32 v20, v20, s1, v23
	v_mov_b32_e32 v32, 0
	v_cvt_pk_fp8_f32 v32, v15, v20
	v_mul_f32_e32 v27, s5, v57
	v_mul_f32_e32 v20, s5, v53
	v_med3_f32 v15, v27, s1, v23
	v_med3_f32 v20, v20, s1, v23
	v_cvt_pk_fp8_f32 v32, v15, v20 op_sel:[0,0,1]
	v_lshl_add_u32 v29, v62, 4, v59
	v_or_b32_e32 v14, v29, v18
	v_lshl_add_u32 v31, v63, 4, v59
	ds_write_b32 v14, v24 offset:512
	v_or_b32_e32 v14, v31, v18
	s_add_i32 s1, s4, 0x2001
	ds_write_b32 v14, v32 offset:768
	s_cbranch_vccz .LBB0_982
	s_lshr_b32 s12, s4, 4
	s_lshl_b32 s5, s1, 6
	s_lshl_b64 s[18:19], s[12:13], 20
	s_and_b32 s5, s5, 0x340
	s_lshl_b64 s[14:15], s[12:13], 18
	v_lshl_add_u64 v[14:15], v[6:7], 0, s[18:19]
	s_lshl_b32 s12, s5, 2
	v_lshl_add_u64 v[14:15], v[14:15], 0, s[12:13]
	s_add_u32 s12, s42, s14
	s_addc_u32 s13, s43, s15
	s_lshl_b32 s5, s5, 8
	s_add_u32 s14, s12, s5
	v_lshl_add_u64 v[14:15], v[14:15], 0, v[8:9]
	s_addc_u32 s15, s13, 0
	v_and_or_b32 v20, v16, 56, v17
	s_andn2_b64 vcc, exec, s[16:17]
	v_lshlrev_b32_e32 v16, 2, v12
	s_cbranch_vccz .LBB0_983
	s_mov_b32 s1, 0x42800000
	s_mov_b64 s[12:13], 0x100
	s_mov_b64 s[18:19], 0x400
	s_branch .LBB0_984

; __device__ __forceinline__ int otid() { int t = threadIdx.x; asm volatile("" : "+v"(t)); return t; }
; #define CV_MULG(r, g) do { r.x *= g; r.y *= g; r.z *= g; r.w *= g; } while (0)
; __device__ void conv_jobs(const Params& p, unsigned char* smem, int job0, int jstride, int njobs) {
;     const int tid = otid();
;     float4 r0, r1, r2, r3, r4, r5, r6, r7;
;     int job = job0;
;     if (job >= njobs) return;
;     ConvJob cur = conv_job_decode(p, job, tid);
;     CV_LOAD(cur, r0, r1, r2, r3, r4, r5, r6, r7);
;     for (int it = 0;; ++it) {
;         unsigned char* tile = smem + (it & 1) * 16384;
;         if (cur.gain) { const float* g_ = cur.gain; const float g0 = g_[0], g1 = g_[1], g2 = g_[2], g3 = g_[3], g4 = g_[128], g5 = g_[129], g6 = g_[130], g7 = g_[131];
;     ...
;             CV_MULG(r0, g0); CV_MULG(r1, g1); CV_MULG(r2, g2); CV_MULG(r3, g3); CV_MULG(r4, g4); CV_MULG(r5, g5); CV_MULG(r6, g6); CV_MULG(r7, g7);
;     ...
;         }
;         CV_PUT(tile, cur, r0, r1, r2, r3, r4, r5, r6, r7);
;         const int nj = job + jstride;
;         const bool more = nj < njobs;
;         ConvJob nxt = cur;
;         if (more) { nxt = conv_job_decode(p, nj, tid); CV_LOAD(nxt, r0, r1, r2, r3, r4, r5, r6, r7); }
;         __syncthreads();
;         CV_OUT(tile, cur);
;         if (!more) break;
;         cur = nxt; job = nj;
;     }
;     __syncthreads();
.LBB0_1019:
	s_lshl_b32 s16, s14, 2
	v_lshl_add_u64 v[10:11], v[6:7], 0, s[16:17]
	global_load_dwordx4 v[2:5], v[6:7], off nt
	s_mulk_i32 s14, 0x1f4
	global_load_dwordx4 v[6:9], v[10:11], off nt
	v_lshl_add_u64 v[10:11], v[10:11], 0, s[16:17]
	global_load_dwordx4 v[16:19], v[10:11], off nt
	v_lshl_add_u64 v[10:11], v[10:11], 0, s[16:17]
	s_mov_b32 s15, s17
	global_load_dwordx4 v[32:35], v[10:11], off nt
	v_lshl_add_u64 v[10:11], v[10:11], 0, s[14:15]
	global_load_dwordx4 v[36:39], v[10:11], off nt
	v_lshl_add_u64 v[10:11], v[10:11], 0, s[16:17]
	global_load_dwordx4 v[40:43], v[10:11], off nt
	v_lshl_add_u64 v[10:11], v[10:11], 0, s[16:17]
	global_load_dwordx4 v[44:47], v[10:11], off nt
	v_lshl_add_u64 v[10:11], v[10:11], 0, s[16:17]
	global_load_dwordx4 v[48:51], v[10:11], off nt
	s_waitcnt lgkmcnt(0)
	s_barrier
	ds_read_b128 v[52:55], v22
	ds_read_b128 v[56:59], v21
	v_mov_b64_e32 v[10:11], s[10:11]
	v_mad_u64_u32 v[10:11], s[8:9], s8, v20, v[10:11]
	s_mov_b32 s5, 0xc3dc0000
	v_mov_b32_e32 v31, 0x43dc0000
	v_lshl_add_u64 v[60:61], v[10:11], 0, v[12:13]
	v_lshl_add_u64 v[10:11], v[10:11], 0, v[14:15]
	v_mov_b32_e32 v63, 0
	v_mov_b32_e32 v65, 0
	v_mov_b32_e32 v66, 0
	s_waitcnt lgkmcnt(1)
	global_store_dwordx4 v[60:61], v[52:55], off
	s_waitcnt lgkmcnt(0)
	global_store_dwordx4 v[10:11], v[56:59], off
	v_mov_b32_e32 v64, 0
	v_mov_b32_e32 v67, 0
	v_mov_b32_e32 v62, 0
	s_waitcnt vmcnt(9)
	v_mul_f32_e32 v2, s4, v2
	v_mul_f32_e32 v4, s4, v4
	v_mul_f32_e32 v5, s4, v5
	s_waitcnt vmcnt(8)
	v_mul_f32_e32 v6, s4, v6
	v_mul_f32_e32 v8, s4, v8
	v_mul_f32_e32 v9, s4, v9
	v_mul_f32_e32 v3, s4, v3
	v_med3_f32 v2, v2, s5, v31
	v_med3_f32 v4, v4, s5, v31
	v_med3_f32 v5, v5, s5, v31
	v_mul_f32_e32 v7, s4, v7
	v_med3_f32 v6, v6, s5, v31
	s_waitcnt vmcnt(7)
	v_mul_f32_e32 v11, s4, v17
	v_med3_f32 v8, v8, s5, v31
	v_med3_f32 v9, v9, s5, v31
	v_med3_f32 v3, v3, s5, v31
	v_med3_f32 v7, v7, s5, v31
	v_cvt_pk_fp8_f32 v63, v2, v6
	v_med3_f32 v2, v11, s5, v31
	v_cvt_pk_fp8_f32 v65, v4, v8
	v_cvt_pk_fp8_f32 v66, v5, v9
	s_waitcnt vmcnt(5)
	v_mul_f32_e32 v9, s4, v36
	s_waitcnt vmcnt(4)
	v_mul_f32_e32 v11, s4, v40
	v_cvt_pk_fp8_f32 v64, v3, v7
	v_med3_f32 v9, v9, s5, v31
	v_med3_f32 v11, v11, s5, v31
	v_mul_f32_e32 v10, s4, v16
	v_mul_f32_e32 v16, s4, v18
	v_mul_f32_e32 v7, s4, v34
	v_cvt_pk_fp8_f32 v67, v9, v11
	v_mul_f32_e32 v6, s4, v33
	v_med3_f32 v3, v16, s5, v31
	v_med3_f32 v7, v7, s5, v31
	v_med3_f32 v6, v6, s5, v31
	s_waitcnt vmcnt(3)
	v_mul_f32_e32 v16, s4, v44
	v_cvt_pk_fp8_f32 v65, v3, v7 op_sel:[0,0,1]
	s_waitcnt vmcnt(2)
	v_mul_f32_e32 v3, s4, v48
	v_mul_f32_e32 v18, s4, v32
	v_cvt_pk_fp8_f32 v64, v2, v6 op_sel:[0,0,1]
	v_med3_f32 v2, v16, s5, v31
	v_med3_f32 v3, v3, s5, v31
	v_med3_f32 v10, v10, s5, v31
	v_med3_f32 v5, v18, s5, v31
	v_cvt_pk_fp8_f32 v67, v2, v3 op_sel:[0,0,1]
	v_mul_f32_e32 v2, s4, v37
	v_mul_f32_e32 v3, s4, v41
	v_cvt_pk_fp8_f32 v63, v10, v5 op_sel:[0,0,1]
	v_med3_f32 v2, v2, s5, v31
	v_med3_f32 v3, v3, s5, v31
	v_mov_b32_e32 v5, 0
	v_mul_f32_e32 v17, s4, v19
	v_mul_f32_e32 v8, s4, v35
	v_cvt_pk_fp8_f32 v5, v2, v3
	v_med3_f32 v4, v17, s5, v31
	v_med3_f32 v8, v8, s5, v31
	v_cvt_pk_fp8_f32 v66, v4, v8 op_sel:[0,0,1]
	v_mul_f32_e32 v4, s4, v45
	v_mul_f32_e32 v3, s4, v49
	v_med3_f32 v2, v4, s5, v31
	v_med3_f32 v3, v3, s5, v31
	v_cvt_pk_fp8_f32 v5, v2, v3 op_sel:[0,0,1]
	v_mul_f32_e32 v2, s4, v38
	v_mul_f32_e32 v3, s4, v42
	v_med3_f32 v2, v2, s5, v31
	v_med3_f32 v3, v3, s5, v31
	v_mov_b32_e32 v6, 0
	v_cvt_pk_fp8_f32 v6, v2, v3
	v_mul_f32_e32 v4, s4, v46
	v_mul_f32_e32 v3, s4, v50
	v_med3_f32 v2, v4, s5, v31
	v_med3_f32 v3, v3, s5, v31
	v_cvt_pk_fp8_f32 v6, v2, v3 op_sel:[0,0,1]
	v_mul_f32_e32 v2, s4, v39
	v_mul_f32_e32 v3, s4, v43
	v_med3_f32 v2, v2, s5, v31
	v_med3_f32 v3, v3, s5, v31
	v_cvt_pk_fp8_f32 v62, v2, v3
	v_mul_f32_e32 v4, s4, v47
	v_mul_f32_e32 v3, s4, v51
	v_med3_f32 v2, v4, s5, v31
	v_med3_f32 v3, v3, s5, v31
	v_cvt_pk_fp8_f32 v62, v2, v3 op_sel:[0,0,1]
	ds_write_b32 v23, v63 offset:16384
	ds_write_b32 v24, v64 offset:16640
	ds_write_b32 v27, v65 offset:16896
	ds_write_b32 v28, v66 offset:17152
	ds_write_b32 v25, v67 offset:16384
	ds_write_b32 v26, v5 offset:16640
	ds_write_b32 v29, v6 offset:16896
	ds_write_b32 v30, v62 offset:17152
	s_waitcnt lgkmcnt(0)
	s_barrier
	ds_read_b128 v[2:5], v22 offset:16384
	ds_read_b128 v[6:9], v21 offset:16384
	v_mov_b64_e32 v[10:11], s[0:1]
	v_mad_u64_u32 v[10:11], s[0:1], s12, v20, v[10:11]
	v_lshl_add_u64 v[12:13], v[10:11], 0, v[12:13]
	s_waitcnt lgkmcnt(1)
	global_store_dwordx4 v[12:13], v[2:5], off
	s_nop 1
	v_lshl_add_u64 v[2:3], v[10:11], 0, v[14:15]
	s_waitcnt lgkmcnt(0)
	global_store_dwordx4 v[2:3], v[6:9], off
	s_barrier

; __device__ __forceinline__ ConvJob conv_job_decode(const Params& p, int job, int tid) {
;     ...
;         const int q = job - 8192, e = q >> 4, ng = q & 15;
;         j.sp = p.we_down + (size_t)e * 262144 + (size_t)kr * 1024 + ng * 64 + n4; j.ldsrc = 1024;
;         j.dst8 = p.dT8 + (size_t)e * 262144 + (size_t)(ng * 64) * 256; j.ld8 = 256; j.s8 = D8S;
.LBB0_1085:
	s_lshl_b32 s1, s0, 2
	s_mul_i32 s8, s0, 0x20c
	s_sub_u32 s38, 0, s1
	v_lshl_add_u64 v[18:19], v[12:13], 0, s[8:9]
	s_subb_u32 s39, 0, 0
	v_lshl_add_u64 v[24:25], v[18:19], 0, s[38:39]
	v_lshl_add_u64 v[14:15], v[24:25], 0, s[38:39]
	v_lshl_add_u64 v[26:27], v[14:15], 0, s[38:39]
	global_load_dwordx4 v[14:17], v[14:15], off nt
	s_nop 0
	global_load_dwordx4 v[34:37], v[26:27], off nt
	v_mad_i64_i32 v[26:27], s[0:1], s0, v21, v[26:27]
	global_load_dwordx4 v[30:33], v[26:27], off nt
	v_lshl_add_u64 v[26:27], v[26:27], 0, s[38:39]
	global_load_dwordx4 v[38:41], v[26:27], off nt
	v_lshl_add_u64 v[26:27], v[26:27], 0, s[38:39]
	global_load_dwordx4 v[42:45], v[12:13], off nt
	global_load_dwordx4 v[46:49], v[26:27], off nt
	global_load_dwordx4 v[50:53], v[18:19], off nt
	global_load_dwordx4 v[54:57], v[24:25], off nt
	v_mov_b32_e32 v25, 0
	v_mov_b32_e32 v26, 0
	v_mov_b32_e32 v27, 0
	s_waitcnt vmcnt(19)
	v_mov_b32_e32 v58, 0
	v_ashrrev_i32_e32 v11, 4, v9
	v_lshrrev_b32_e32 v12, 2, v10
	v_ashrrev_i32_e32 v19, 6, v9
	v_add_u32_e32 v23, 32, v11
	v_lshlrev_b32_e32 v11, 2, v11
	v_xor_b32_e32 v28, 4, v12
	v_lshlrev_b32_e32 v13, 8, v10
	v_xor_b32_e32 v24, v12, v19
	v_xor_b32_e32 v29, 8, v12
	v_xor_b32_e32 v59, 12, v12
	v_and_b32_e32 v18, 12, v11
	v_xor_b32_e32 v11, v28, v19
	v_ashrrev_i32_e32 v23, 2, v23
	v_xor_b32_e32 v60, v29, v19
	v_xor_b32_e32 v61, v59, v19
	v_lshl_add_u32 v24, v24, 4, v13
	v_xor_b32_e32 v12, v23, v12
	v_xor_b32_e32 v62, v28, v23
	v_xor_b32_e32 v63, v29, v23
	v_xor_b32_e32 v59, v59, v23
	v_lshl_add_u32 v23, v11, 4, v13
	v_or_b32_e32 v64, v24, v18
	v_lshl_add_u32 v28, v60, 4, v13
	v_lshl_add_u32 v29, v61, 4, v13
	v_or_b32_e32 v11, v23, v18
	v_or_b32_e32 v60, v28, v18
	v_or_b32_e32 v61, v29, v18
	v_cmp_gt_u32_e64 s[0:1], 32, v10
	v_lshl_add_u64 v[6:7], s[48:49], 0, v[6:7]
	s_add_i32 s21, s5, 0x2001
	s_and_b64 vcc, exec, s[18:19]
	s_waitcnt vmcnt(7)
	v_mul_f32_e32 v14, s30, v14
	s_waitcnt vmcnt(6)
	v_mul_f32_e32 v34, s30, v34
	v_med3_f32 v34, v34, s4, v22
	s_waitcnt vmcnt(5)
	v_mul_f32_e32 v30, s30, v30
	v_mul_f32_e32 v31, s30, v31
	s_waitcnt vmcnt(4)
	v_mul_f32_e32 v38, s30, v38
	s_waitcnt vmcnt(3)
	v_mul_f32_e32 v42, s30, v42
	s_waitcnt vmcnt(2)
	v_mul_f32_e32 v46, s30, v46
	v_mul_f32_e32 v43, s30, v43
	v_mul_f32_e32 v47, s30, v47
	v_med3_f32 v42, v42, s4, v22
	v_med3_f32 v46, v46, s4, v22
	v_mul_f32_e32 v44, s30, v44
	v_mul_f32_e32 v48, s30, v48
	v_med3_f32 v43, v43, s4, v22
	v_med3_f32 v47, v47, s4, v22
	v_cvt_pk_fp8_f32 v25, v42, v46
	v_mul_f32_e32 v45, s30, v45
	v_mul_f32_e32 v49, s30, v49
	v_med3_f32 v44, v44, s4, v22
	v_med3_f32 v48, v48, s4, v22
	v_cvt_pk_fp8_f32 v26, v43, v47
	v_med3_f32 v45, v45, s4, v22
	v_med3_f32 v49, v49, s4, v22
	v_cvt_pk_fp8_f32 v27, v44, v48
	v_med3_f32 v30, v30, s4, v22
	v_mul_f32_e32 v39, s30, v39
	v_med3_f32 v38, v38, s4, v22
	v_cvt_pk_fp8_f32 v58, v45, v49
	v_mul_f32_e32 v32, s30, v32
	v_med3_f32 v31, v31, s4, v22
	v_mul_f32_e32 v40, s30, v40
	v_med3_f32 v39, v39, s4, v22
	v_cvt_pk_fp8_f32 v25, v38, v30 op_sel:[0,0,1]
	v_mul_f32_e32 v33, s30, v33
	v_med3_f32 v32, v32, s4, v22
	v_mul_f32_e32 v41, s30, v41
	v_med3_f32 v40, v40, s4, v22
	v_cvt_pk_fp8_f32 v26, v39, v31 op_sel:[0,0,1]
	v_med3_f32 v33, v33, s4, v22
	v_med3_f32 v41, v41, s4, v22
	v_cvt_pk_fp8_f32 v27, v40, v32 op_sel:[0,0,1]
	v_cvt_pk_fp8_f32 v58, v41, v33 op_sel:[0,0,1]
	ds_write_b32 v64, v25
	ds_write_b32 v11, v26 offset:256
	ds_write_b32 v60, v27 offset:512
	ds_write_b32 v61, v58 offset:768
	v_med3_f32 v11, v14, s4, v22
	v_mov_b32_e32 v25, 0
	v_cvt_pk_fp8_f32 v25, v34, v11
	s_waitcnt vmcnt(0)
	v_mul_f32_e32 v14, s30, v54
	v_med3_f32 v11, v14, s4, v22
	v_mul_f32_e32 v14, s30, v50
	v_med3_f32 v14, v14, s4, v22
	v_cvt_pk_fp8_f32 v25, v11, v14 op_sel:[0,0,1]
	v_lshl_add_u32 v32, v12, 4, v13
	v_mul_f32_e32 v12, s30, v35
	v_mul_f32_e32 v14, s30, v15
	v_med3_f32 v12, v12, s4, v22
	v_med3_f32 v14, v14, s4, v22
	v_mov_b32_e32 v26, 0
	v_cvt_pk_fp8_f32 v26, v12, v14
	v_mul_f32_e32 v15, s30, v55
	v_mul_f32_e32 v14, s30, v51
	v_med3_f32 v12, v15, s4, v22
	v_med3_f32 v14, v14, s4, v22
	v_cvt_pk_fp8_f32 v26, v12, v14 op_sel:[0,0,1]
	v_or_b32_e32 v11, v32, v18
	v_lshl_add_u32 v34, v62, 4, v13
	ds_write_b32 v11, v25
	v_or_b32_e32 v11, v34, v18
	ds_write_b32 v11, v26 offset:256
	v_mul_f32_e32 v11, s30, v36
	v_mul_f32_e32 v12, s30, v16
	v_med3_f32 v11, v11, s4, v22
	v_med3_f32 v12, v12, s4, v22
	v_mov_b32_e32 v15, 0
	v_cvt_pk_fp8_f32 v15, v11, v12
	v_mul_f32_e32 v14, s30, v56
	v_mul_f32_e32 v12, s30, v52
	v_med3_f32 v11, v14, s4, v22
	v_med3_f32 v12, v12, s4, v22
	v_cvt_pk_fp8_f32 v15, v11, v12 op_sel:[0,0,1]
	v_mul_f32_e32 v12, s30, v37
	v_mul_f32_e32 v14, s30, v17
	v_med3_f32 v12, v12, s4, v22
	v_med3_f32 v14, v14, s4, v22
	v_mov_b32_e32 v17, 0
	v_cvt_pk_fp8_f32 v17, v12, v14
	v_mul_f32_e32 v16, s30, v57
	v_mul_f32_e32 v14, s30, v53
	v_med3_f32 v12, v16, s4, v22
	v_med3_f32 v14, v14, s4, v22
	v_cvt_pk_fp8_f32 v17, v12, v14 op_sel:[0,0,1]
	v_lshl_add_u32 v33, v63, 4, v13
	v_or_b32_e32 v11, v33, v18
	v_lshl_add_u32 v35, v59, 4, v13
	ds_write_b32 v11, v15 offset:512
	v_or_b32_e32 v11, v35, v18
	v_lshlrev_b32_e32 v12, 2, v10
	ds_write_b32 v11, v17 offset:768
	s_cbranch_vccz .LBB0_1087
	s_lshr_b32 s8, s5, 4
	s_lshl_b64 s[30:31], s[8:9], 18
	s_lshl_b64 s[38:39], s[8:9], 20
	s_lshl_b32 s8, s21, 6
	v_lshl_add_u64 v[10:11], v[6:7], 0, s[38:39]
	s_and_b32 s38, s8, 0x340
	s_lshl_b32 s8, s38, 2
	v_lshl_add_u64 v[10:11], v[10:11], 0, s[8:9]
	s_add_u32 s8, s42, s30
	s_addc_u32 s30, s43, s31
	s_lshl_b32 s31, s38, 8
	v_mov_b32_e32 v13, v3
	s_add_u32 s54, s8, s31
	v_lshl_add_u64 v[10:11], v[10:11], 0, v[12:13]
	s_addc_u32 s55, s30, 0
	s_mov_b64 s[38:39], 0
	s_branch .LBB0_1088

; __device__ __forceinline__ int otid() { int t = threadIdx.x; asm volatile("" : "+v"(t)); return t; }
; #define CV_MULG(r, g) do { r.x *= g; r.y *= g; r.z *= g; r.w *= g; } while (0)
; __device__ void conv_jobs(const Params& p, unsigned char* smem, int job0, int jstride, int njobs) {
;     const int tid = otid();
;     float4 r0, r1, r2, r3, r4, r5, r6, r7;
;     int job = job0;
;     if (job >= njobs) return;
;     ConvJob cur = conv_job_decode(p, job, tid);
;     CV_LOAD(cur, r0, r1, r2, r3, r4, r5, r6, r7);
;     for (int it = 0;; ++it) {
;         unsigned char* tile = smem + (it & 1) * 16384;
;         if (cur.gain) { const float* g_ = cur.gain; const float g0 = g_[0], g1 = g_[1], g2 = g_[2], g3 = g_[3], g4 = g_[128], g5 = g_[129], g6 = g_[130], g7 = g_[131];
;     ...
;             CV_MULG(r0, g0); CV_MULG(r1, g1); CV_MULG(r2, g2); CV_MULG(r3, g3); CV_MULG(r4, g4); CV_MULG(r5, g5); CV_MULG(r6, g6); CV_MULG(r7, g7);
;     ...
;         }
;         CV_PUT(tile, cur, r0, r1, r2, r3, r4, r5, r6, r7);
;         const int nj = job + jstride;
;         const bool more = nj < njobs;
;         ConvJob nxt = cur;
;         if (more) { nxt = conv_job_decode(p, nj, tid); CV_LOAD(nxt, r0, r1, r2, r3, r4, r5, r6, r7); }
;         __syncthreads();
;         CV_OUT(tile, cur);
;         if (!more) break;
;         cur = nxt; job = nj;
.LBB0_1091:
	s_lshl_b32 s8, s0, 2
	global_load_dwordx4 v[36:39], v[10:11], off nt
	v_lshl_add_u64 v[10:11], v[10:11], 0, s[8:9]
	global_load_dwordx4 v[40:43], v[10:11], off nt
	v_lshl_add_u64 v[10:11], v[10:11], 0, s[8:9]
	global_load_dwordx4 v[44:47], v[10:11], off nt
	v_lshl_add_u64 v[10:11], v[10:11], 0, s[8:9]
	global_load_dwordx4 v[48:51], v[10:11], off nt
	s_mulk_i32 s0, 0x1f4
	s_mov_b32 s1, s9
	v_lshrrev_b32_e32 v13, 3, v9
	v_and_b32_e32 v15, 7, v9
	v_lshrrev_b32_e32 v25, 2, v9
	v_bfe_u32 v52, v9, 5, 1
	v_lshl_add_u64 v[10:11], v[10:11], 0, s[0:1]
	v_add_u32_e32 v27, v23, v18
	v_and_or_b32 v23, v13, 56, v15
	v_and_or_b32 v13, v25, 6, v52
	global_load_dwordx4 v[52:55], v[10:11], off nt
	v_lshl_add_u64 v[10:11], v[10:11], 0, s[8:9]
	global_load_dwordx4 v[56:59], v[10:11], off nt
	v_lshl_add_u64 v[10:11], v[10:11], 0, s[8:9]
	global_load_dwordx4 v[60:63], v[10:11], off nt
	v_lshl_add_u64 v[10:11], v[10:11], 0, s[8:9]
	global_load_dwordx4 v[64:67], v[10:11], off nt
	v_add_u32_e32 v9, 0x200, v9
	v_ashrrev_i32_e32 v9, 6, v9
	v_lshrrev_b32_e32 v15, 2, v23
	v_and_or_b32 v11, v19, -8, v13
	v_and_or_b32 v9, v9, -8, v13
	v_xor_b32_e32 v13, v15, v8
	v_xor_b32_e32 v15, v13, v11
	v_add_u32_e32 v26, v24, v18
	v_lshlrev_b32_e32 v24, 8, v23
	v_lshlrev_b32_e32 v8, 4, v9
	v_xor_b32_e32 v9, v13, v9
	v_lshlrev_b32_e32 v13, 4, v15
	v_lshlrev_b32_e32 v9, 4, v9
	v_add_u32_e32 v25, v24, v13
	v_add_u32_e32 v24, v24, v9
	s_waitcnt lgkmcnt(0)
	s_barrier
	ds_read_b128 v[68:71], v25
	ds_read_b128 v[72:75], v24
	v_mov_b64_e32 v[30:31], s[22:23]
	v_lshlrev_b32_e32 v10, 4, v11
	v_mad_u64_u32 v[30:31], s[0:1], s20, v23, v[30:31]
	v_ashrrev_i32_e32 v11, 31, v10
	v_ashrrev_i32_e32 v9, 31, v8
	v_lshl_add_u64 v[76:77], v[30:31], 0, v[10:11]
	v_lshl_add_u64 v[30:31], v[30:31], 0, v[8:9]
	v_mov_b32_e32 v79, 0
	s_waitcnt lgkmcnt(1)
	global_store_dwordx4 v[76:77], v[68:71], off
	s_waitcnt lgkmcnt(0)
	global_store_dwordx4 v[30:31], v[72:75], off
	v_mov_b32_e32 v78, 0
	v_mov_b32_e32 v80, 0
	s_andn2_b64 vcc, exec, s[18:19]
	s_add_i32 s22, s5, 0x2002
	s_waitcnt vmcnt(9)
	v_mul_f32_e32 v13, s21, v36
	v_mul_f32_e32 v15, s21, v37
	s_waitcnt vmcnt(8)
	v_mul_f32_e32 v36, s21, v41
	v_mul_f32_e32 v19, s21, v38
	v_med3_f32 v15, v15, s4, v22
	v_mul_f32_e32 v31, s21, v40
	v_mul_f32_e32 v37, s21, v42
	v_med3_f32 v36, v36, s4, v22
	v_med3_f32 v13, v13, s4, v22
	v_med3_f32 v19, v19, s4, v22
	v_med3_f32 v31, v31, s4, v22
	v_med3_f32 v37, v37, s4, v22
	v_cvt_pk_fp8_f32 v79, v15, v36
	v_cvt_pk_fp8_f32 v78, v13, v31
	v_cvt_pk_fp8_f32 v80, v19, v37
	s_waitcnt vmcnt(7)
	v_mul_f32_e32 v40, s21, v45
	s_waitcnt vmcnt(6)
	v_mul_f32_e32 v31, s21, v49
	v_mul_f32_e32 v30, s21, v39
	v_mul_f32_e32 v39, s21, v44
	v_mul_f32_e32 v41, s21, v46
	v_mul_f32_e32 v42, s21, v48
	v_med3_f32 v13, v40, s4, v22
	v_mul_f32_e32 v36, s21, v50
	v_med3_f32 v31, v31, s4, v22
	v_mul_f32_e32 v38, s21, v43
	v_med3_f32 v39, v39, s4, v22
	v_med3_f32 v15, v41, s4, v22
	v_med3_f32 v19, v42, s4, v22
	v_cvt_pk_fp8_f32 v79, v13, v31 op_sel:[0,0,1]
	v_med3_f32 v13, v36, s4, v22
	v_med3_f32 v30, v30, s4, v22
	v_cvt_pk_fp8_f32 v78, v39, v19 op_sel:[0,0,1]
	v_cvt_pk_fp8_f32 v80, v15, v13 op_sel:[0,0,1]
	v_med3_f32 v13, v38, s4, v22
	v_mov_b32_e32 v19, 0
	v_cvt_pk_fp8_f32 v19, v30, v13
	v_mul_f32_e32 v15, s21, v47
	v_med3_f32 v13, v15, s4, v22
	v_mul_f32_e32 v15, s21, v51
	v_med3_f32 v15, v15, s4, v22
	v_cvt_pk_fp8_f32 v19, v13, v15 op_sel:[0,0,1]
	s_waitcnt vmcnt(5)
	v_mul_f32_e32 v13, s21, v52
	s_waitcnt vmcnt(4)
	v_mul_f32_e32 v15, s21, v56
	v_add_u32_e32 v31, v29, v18
	v_med3_f32 v13, v13, s4, v22
	v_med3_f32 v15, v15, s4, v22
	v_mov_b32_e32 v29, 0
	v_cvt_pk_fp8_f32 v29, v13, v15
	v_add_u32_e32 v30, v28, v18
	ds_write_b32 v26, v78 offset:16384
	ds_write_b32 v27, v79 offset:16640
	ds_write_b32 v30, v80 offset:16896
	ds_write_b32 v31, v19 offset:17152
	s_waitcnt vmcnt(3)
	v_mul_f32_e32 v19, s21, v60
	s_waitcnt vmcnt(2)
	v_mul_f32_e32 v15, s21, v64
	v_med3_f32 v13, v19, s4, v22
	v_med3_f32 v15, v15, s4, v22
	v_cvt_pk_fp8_f32 v29, v13, v15 op_sel:[0,0,1]
	v_mul_f32_e32 v13, s21, v53
	v_mul_f32_e32 v15, s21, v57
	v_med3_f32 v13, v13, s4, v22
	v_med3_f32 v15, v15, s4, v22
	v_mov_b32_e32 v36, 0
	v_cvt_pk_fp8_f32 v36, v13, v15
	v_mul_f32_e32 v19, s21, v61
	v_mul_f32_e32 v15, s21, v65
	v_med3_f32 v13, v19, s4, v22
	v_med3_f32 v15, v15, s4, v22
	v_cvt_pk_fp8_f32 v36, v13, v15 op_sel:[0,0,1]
	v_add_u32_e32 v28, v32, v18
	v_mul_f32_e32 v13, s21, v54
	v_mul_f32_e32 v15, s21, v58
	ds_write_b32 v28, v29 offset:16384
	v_add_u32_e32 v29, v34, v18
	v_med3_f32 v13, v13, s4, v22
	v_med3_f32 v15, v15, s4, v22
	v_mov_b32_e32 v34, 0
	v_cvt_pk_fp8_f32 v34, v13, v15
	v_mul_f32_e32 v19, s21, v62
	v_mul_f32_e32 v15, s21, v66
	v_med3_f32 v13, v19, s4, v22
	v_med3_f32 v15, v15, s4, v22
	v_cvt_pk_fp8_f32 v34, v13, v15 op_sel:[0,0,1]
	v_mul_f32_e32 v13, s21, v55
	v_mul_f32_e32 v15, s21, v59
	ds_write_b32 v29, v36 offset:16640
	v_med3_f32 v13, v13, s4, v22
	v_med3_f32 v15, v15, s4, v22
	v_mov_b32_e32 v36, 0
	v_cvt_pk_fp8_f32 v36, v13, v15
	v_mul_f32_e32 v19, s21, v63
	v_mul_f32_e32 v15, s21, v67
	v_med3_f32 v13, v19, s4, v22
	v_med3_f32 v15, v15, s4, v22
	v_cvt_pk_fp8_f32 v36, v13, v15 op_sel:[0,0,1]
	v_cndmask_b32_e64 v13, 0, 1, s[18:19]
	v_add_u32_e32 v32, v33, v18
	v_add_u32_e32 v33, v35, v18
	v_cmp_ne_u32_e64 s[0:1], 1, v13
	ds_write_b32 v32, v34 offset:16896
	ds_write_b32 v33, v36 offset:17152
	s_cbranch_vccnz .LBB0_1094
	s_lshr_b32 s8, s5, 4
	s_lshl_b64 s[18:19], s[8:9], 18
	s_lshl_b64 s[20:21], s[8:9], 20
	s_lshl_b32 s8, s22, 6
	v_lshl_add_u64 v[18:19], v[6:7], 0, s[20:21]
	s_and_b32 s20, s8, 0x380
	s_lshl_b32 s8, s20, 2
	v_lshl_add_u64 v[18:19], v[18:19], 0, s[8:9]
	s_add_u32 s8, s42, s18
	s_addc_u32 s18, s43, s19
	s_lshl_b32 s19, s20, 8
	v_mov_b32_e32 v13, v3
	s_add_u32 s20, s8, s19
	v_lshl_add_u64 v[18:19], v[18:19], 0, v[12:13]
	s_addc_u32 s21, s18, 0
	s_cbranch_execz .LBB0_1095
	s_mov_b32 s30, 0x42800000
	s_mov_b64 s[18:19], 0x100
	s_mov_b64 s[22:23], 0x400
	s_branch .LBB0_1096

; __device__ __forceinline__ int otid() { int t = threadIdx.x; asm volatile("" : "+v"(t)); return t; }
; #define CV_MULG(r, g) do { r.x *= g; r.y *= g; r.z *= g; r.w *= g; } while (0)
; __device__ void conv_jobs(const Params& p, unsigned char* smem, int job0, int jstride, int njobs) {
;     const int tid = otid();
;     float4 r0, r1, r2, r3, r4, r5, r6, r7;
;     int job = job0;
;     if (job >= njobs) return;
;     ConvJob cur = conv_job_decode(p, job, tid);
;     CV_LOAD(cur, r0, r1, r2, r3, r4, r5, r6, r7);
;     for (int it = 0;; ++it) {
;         unsigned char* tile = smem + (it & 1) * 16384;
;         if (cur.gain) { const float* g_ = cur.gain; const float g0 = g_[0], g1 = g_[1], g2 = g_[2], g3 = g_[3], g4 = g_[128], g5 = g_[129], g6 = g_[130], g7 = g_[131];
;     ...
;             CV_MULG(r0, g0); CV_MULG(r1, g1); CV_MULG(r2, g2); CV_MULG(r3, g3); CV_MULG(r4, g4); CV_MULG(r5, g5); CV_MULG(r6, g6); CV_MULG(r7, g7);
;     ...
;         }
;         CV_PUT(tile, cur, r0, r1, r2, r3, r4, r5, r6, r7);
;         const int nj = job + jstride;
;         const bool more = nj < njobs;
;         ConvJob nxt = cur;
;         if (more) { nxt = conv_job_decode(p, nj, tid); CV_LOAD(nxt, r0, r1, r2, r3, r4, r5, r6, r7); }
;         __syncthreads();
;         CV_OUT(tile, cur);
;         if (!more) break;
;         cur = nxt; job = nj;
.LBB0_1096:
	s_lshl_b32 s8, s22, 2
	global_load_dwordx4 v[34:37], v[18:19], off nt
	v_lshl_add_u64 v[18:19], v[18:19], 0, s[8:9]
	global_load_dwordx4 v[38:41], v[18:19], off nt
	v_lshl_add_u64 v[18:19], v[18:19], 0, s[8:9]
	global_load_dwordx4 v[42:45], v[18:19], off nt
	v_lshl_add_u64 v[18:19], v[18:19], 0, s[8:9]
	global_load_dwordx4 v[46:49], v[18:19], off nt
	s_mulk_i32 s22, 0x1f4
	s_mov_b32 s23, s9
	v_lshl_add_u64 v[18:19], v[18:19], 0, s[22:23]
	global_load_dwordx4 v[50:53], v[18:19], off nt
	v_lshl_add_u64 v[18:19], v[18:19], 0, s[8:9]
	global_load_dwordx4 v[54:57], v[18:19], off nt
	v_lshl_add_u64 v[18:19], v[18:19], 0, s[8:9]
	global_load_dwordx4 v[58:61], v[18:19], off nt
	v_lshl_add_u64 v[18:19], v[18:19], 0, s[8:9]
	global_load_dwordx4 v[62:65], v[18:19], off nt
	s_waitcnt lgkmcnt(0)
	s_barrier
	ds_read_b128 v[66:69], v25 offset:16384
	ds_read_b128 v[70:73], v24 offset:16384
	v_mov_b64_e32 v[18:19], s[54:55]
	v_mad_u64_u32 v[18:19], s[22:23], s38, v23, v[18:19]
	v_lshl_add_u64 v[74:75], v[18:19], 0, v[10:11]
	v_lshl_add_u64 v[18:19], v[18:19], 0, v[8:9]
	s_waitcnt lgkmcnt(1)
	global_store_dwordx4 v[74:75], v[66:69], off
	s_waitcnt lgkmcnt(0)
	global_store_dwordx4 v[18:19], v[70:73], off
	v_mov_b32_e32 v13, 0
	v_mov_b32_e32 v15, 0
	v_mov_b32_e32 v76, 0
	v_mov_b32_e32 v77, 0
	v_mov_b32_e32 v78, 0
	s_and_b64 vcc, exec, s[0:1]
	s_add_i32 s19, s5, 0x2003
	s_waitcnt vmcnt(9)
	v_mul_f32_e32 v18, s30, v34
	v_mul_f32_e32 v34, s30, v36
	s_waitcnt vmcnt(8)
	v_mul_f32_e32 v36, s30, v38
	v_mul_f32_e32 v19, s30, v35
	v_mul_f32_e32 v35, s30, v37
	v_med3_f32 v18, v18, s4, v22
	v_mul_f32_e32 v37, s30, v39
	v_med3_f32 v36, v36, s4, v22
	v_med3_f32 v19, v19, s4, v22
	v_mul_f32_e32 v38, s30, v40
	v_med3_f32 v37, v37, s4, v22
	v_cvt_pk_fp8_f32 v13, v18, v36
	v_med3_f32 v34, v34, s4, v22
	v_mul_f32_e32 v39, s30, v41
	v_med3_f32 v38, v38, s4, v22
	v_cvt_pk_fp8_f32 v15, v19, v37
	v_med3_f32 v35, v35, s4, v22
	s_waitcnt vmcnt(7)
	v_mul_f32_e32 v40, s30, v42
	v_mul_f32_e32 v42, s30, v44
	v_med3_f32 v39, v39, s4, v22
	s_waitcnt vmcnt(6)
	v_mul_f32_e32 v44, s30, v46
	v_cvt_pk_fp8_f32 v76, v34, v38
	v_mul_f32_e32 v41, s30, v43
	v_med3_f32 v40, v40, s4, v22
	v_mul_f32_e32 v36, s30, v47
	v_cvt_pk_fp8_f32 v77, v35, v39
	v_med3_f32 v35, v44, s4, v22
	v_med3_f32 v18, v41, s4, v22
	v_mul_f32_e32 v37, s30, v48
	v_med3_f32 v36, v36, s4, v22
	v_cvt_pk_fp8_f32 v13, v40, v35 op_sel:[0,0,1]
	v_mul_f32_e32 v43, s30, v45
	v_med3_f32 v19, v42, s4, v22
	v_mul_f32_e32 v38, s30, v49
	v_med3_f32 v37, v37, s4, v22
	s_waitcnt vmcnt(5)
	v_mul_f32_e32 v39, s30, v50
	s_waitcnt vmcnt(4)
	v_mul_f32_e32 v42, s30, v54
	v_cvt_pk_fp8_f32 v15, v18, v36 op_sel:[0,0,1]
	v_med3_f32 v34, v43, s4, v22
	v_med3_f32 v38, v38, s4, v22
	v_med3_f32 v39, v39, s4, v22
	v_med3_f32 v42, v42, s4, v22
	v_cvt_pk_fp8_f32 v76, v19, v37 op_sel:[0,0,1]
	v_mul_f32_e32 v41, s30, v51
	v_mul_f32_e32 v43, s30, v55
	v_cvt_pk_fp8_f32 v77, v34, v38 op_sel:[0,0,1]
	v_cvt_pk_fp8_f32 v78, v39, v42
	v_med3_f32 v41, v41, s4, v22
	v_med3_f32 v43, v43, s4, v22
	ds_write_b32 v26, v13
	ds_write_b32 v27, v15 offset:256
	ds_write_b32 v30, v76 offset:512
	ds_write_b32 v31, v77 offset:768
	v_mov_b32_e32 v15, 0
	s_waitcnt vmcnt(3)
	v_mul_f32_e32 v44, s30, v58
	s_waitcnt vmcnt(2)
	v_mul_f32_e32 v19, s30, v62
	v_cvt_pk_fp8_f32 v15, v41, v43
	v_med3_f32 v18, v44, s4, v22
	v_med3_f32 v19, v19, s4, v22
	v_cvt_pk_fp8_f32 v78, v18, v19 op_sel:[0,0,1]
	v_mul_f32_e32 v13, s30, v59
	v_mul_f32_e32 v18, s30, v63
	v_med3_f32 v13, v13, s4, v22
	v_med3_f32 v18, v18, s4, v22
	v_cvt_pk_fp8_f32 v15, v13, v18 op_sel:[0,0,1]
	v_mul_f32_e32 v13, s30, v52
	v_mul_f32_e32 v18, s30, v56
	v_med3_f32 v13, v13, s4, v22
	v_med3_f32 v18, v18, s4, v22
	v_mov_b32_e32 v34, 0
	v_cvt_pk_fp8_f32 v34, v13, v18
	v_mul_f32_e32 v19, s30, v60
	v_mul_f32_e32 v18, s30, v64
	v_med3_f32 v13, v19, s4, v22
	v_med3_f32 v18, v18, s4, v22
	v_cvt_pk_fp8_f32 v34, v13, v18 op_sel:[0,0,1]
	v_mul_f32_e32 v13, s30, v53
	v_mul_f32_e32 v18, s30, v57
	v_med3_f32 v13, v13, s4, v22
	v_med3_f32 v18, v18, s4, v22
	v_mov_b32_e32 v35, 0
	v_cvt_pk_fp8_f32 v35, v13, v18
	v_mul_f32_e32 v19, s30, v61
	v_mul_f32_e32 v18, s30, v65
	v_med3_f32 v13, v19, s4, v22
	v_med3_f32 v18, v18, s4, v22
	v_cvt_pk_fp8_f32 v35, v13, v18 op_sel:[0,0,1]
	ds_write_b32 v28, v78
	ds_write_b32 v29, v15 offset:256
	ds_write_b32 v32, v34 offset:512
	ds_write_b32 v33, v35 offset:768
	s_cbranch_vccnz .LBB0_1099
	s_lshr_b32 s8, s5, 4
	s_lshl_b32 s5, s19, 6
	s_and_b32 s5, s5, 0x3c0
	s_lshl_b64 s[0:1], s[8:9], 18
	s_lshl_b64 s[22:23], s[8:9], 20
	s_lshl_b32 s8, s5, 2
	s_add_u32 s0, s42, s0
	v_lshl_add_u64 v[6:7], v[6:7], 0, s[22:23]
	s_addc_u32 s1, s43, s1
	s_lshl_b32 s5, s5, 8
	v_lshl_add_u64 v[6:7], v[6:7], 0, s[8:9]
	v_mov_b32_e32 v13, v3
	s_add_u32 s0, s0, s5
	v_lshl_add_u64 v[6:7], v[6:7], 0, v[12:13]
	s_addc_u32 s1, s1, 0
	s_cbranch_execz .LBB0_1100
	s_mov_b32 s5, 0x42800000
	s_mov_b64 s[22:23], 0x100
	s_mov_b64 s[38:39], 0x400
	s_branch .LBB0_1101

; __device__ __forceinline__ int otid() { int t = threadIdx.x; asm volatile("" : "+v"(t)); return t; }
; #define CV_MULG(r, g) do { r.x *= g; r.y *= g; r.z *= g; r.w *= g; } while (0)
; __device__ void conv_jobs(const Params& p, unsigned char* smem, int job0, int jstride, int njobs) {
;     const int tid = otid();
;     float4 r0, r1, r2, r3, r4, r5, r6, r7;
;     int job = job0;
;     if (job >= njobs) return;
;     ConvJob cur = conv_job_decode(p, job, tid);
;     CV_LOAD(cur, r0, r1, r2, r3, r4, r5, r6, r7);
;     for (int it = 0;; ++it) {
;         unsigned char* tile = smem + (it & 1) * 16384;
;         if (cur.gain) { const float* g_ = cur.gain; const float g0 = g_[0], g1 = g_[1], g2 = g_[2], g3 = g_[3], g4 = g_[128], g5 = g_[129], g6 = g_[130], g7 = g_[131];
;     ...
;             CV_MULG(r0, g0); CV_MULG(r1, g1); CV_MULG(r2, g2); CV_MULG(r3, g3); CV_MULG(r4, g4); CV_MULG(r5, g5); CV_MULG(r6, g6); CV_MULG(r7, g7);
;     ...
;         }
;         CV_PUT(tile, cur, r0, r1, r2, r3, r4, r5, r6, r7);
;         const int nj = job + jstride;
;         const bool more = nj < njobs;
;         ConvJob nxt = cur;
;         if (more) { nxt = conv_job_decode(p, nj, tid); CV_LOAD(nxt, r0, r1, r2, r3, r4, r5, r6, r7); }
;         __syncthreads();
;         CV_OUT(tile, cur);
;         if (!more) break;
;         cur = nxt; job = nj;
;     }
;     __syncthreads();
.LBB0_1101:
	s_lshl_b32 s8, s38, 2
	v_lshl_add_u64 v[16:17], v[6:7], 0, s[8:9]
	v_lshl_add_u64 v[34:35], v[16:17], 0, s[8:9]
	v_lshl_add_u64 v[38:39], v[34:35], 0, s[8:9]
	s_mul_i32 s30, s38, 0x1f4
	s_mov_b32 s31, s9
	global_load_dwordx4 v[12:15], v[6:7], off nt
	v_lshl_add_u64 v[42:43], v[38:39], 0, s[30:31]
	global_load_dwordx4 v[4:7], v[16:17], off nt
	v_lshl_add_u64 v[46:47], v[42:43], 0, s[8:9]
	global_load_dwordx4 v[16:19], v[34:35], off nt
	v_lshl_add_u64 v[50:51], v[46:47], 0, s[8:9]
	global_load_dwordx4 v[34:37], v[38:39], off nt
	v_mov_b32_e32 v66, 0
	global_load_dwordx4 v[38:41], v[42:43], off nt
	v_mov_b32_e32 v67, 0
	global_load_dwordx4 v[42:45], v[46:47], off nt
	v_mov_b32_e32 v68, 0
	global_load_dwordx4 v[46:49], v[50:51], off nt
	v_lshl_add_u64 v[50:51], v[50:51], 0, s[8:9]
	global_load_dwordx4 v[50:53], v[50:51], off nt
	v_mov_b32_e32 v2, 0
	v_mov_b32_e32 v69, 0
	s_waitcnt lgkmcnt(0)
	s_barrier
	ds_read_b128 v[54:57], v25
	ds_read_b128 v[58:61], v24
	v_mov_b64_e32 v[62:63], s[20:21]
	v_mad_u64_u32 v[62:63], s[18:19], s18, v23, v[62:63]
	v_lshl_add_u64 v[64:65], v[62:63], 0, v[10:11]
	v_lshl_add_u64 v[62:63], v[62:63], 0, v[8:9]
	s_waitcnt lgkmcnt(1)
	global_store_dwordx4 v[64:65], v[54:57], off
	s_waitcnt lgkmcnt(0)
	global_store_dwordx4 v[62:63], v[58:61], off
	s_waitcnt vmcnt(9)
	v_mul_f32_e32 v13, s5, v13
	v_mul_f32_e32 v14, s5, v14
	v_mul_f32_e32 v15, s5, v15
	s_waitcnt vmcnt(8)
	v_mul_f32_e32 v5, s5, v5
	v_mul_f32_e32 v6, s5, v6
	v_mul_f32_e32 v7, s5, v7
	v_mul_f32_e32 v12, s5, v12
	v_med3_f32 v13, v13, s4, v22
	v_med3_f32 v14, v14, s4, v22
	v_med3_f32 v15, v15, s4, v22
	v_mul_f32_e32 v4, s5, v4
	v_med3_f32 v5, v5, s4, v22
	v_med3_f32 v6, v6, s4, v22
	s_waitcnt vmcnt(7)
	v_mul_f32_e32 v18, s5, v18
	v_med3_f32 v7, v7, s4, v22
	v_med3_f32 v12, v12, s4, v22
	v_med3_f32 v4, v4, s4, v22
	v_cvt_pk_fp8_f32 v66, v13, v5
	v_med3_f32 v5, v18, s4, v22
	v_cvt_pk_fp8_f32 v67, v14, v6
	v_cvt_pk_fp8_f32 v68, v15, v7
	s_waitcnt vmcnt(5)
	v_mul_f32_e32 v15, s5, v38
	s_waitcnt vmcnt(4)
	v_mul_f32_e32 v18, s5, v42
	v_cvt_pk_fp8_f32 v2, v12, v4
	v_med3_f32 v15, v15, s4, v22
	v_med3_f32 v18, v18, s4, v22
	v_mul_f32_e32 v13, s5, v36
	v_cvt_pk_fp8_f32 v69, v15, v18
	v_mul_f32_e32 v16, s5, v16
	v_mul_f32_e32 v17, s5, v17
	v_mul_f32_e32 v34, s5, v34
	v_mul_f32_e32 v12, s5, v35
	v_med3_f32 v13, v13, s4, v22
	v_mul_f32_e32 v19, s5, v19
	v_med3_f32 v16, v16, s4, v22
	v_med3_f32 v4, v17, s4, v22
	v_med3_f32 v7, v34, s4, v22
	v_med3_f32 v12, v12, s4, v22
	s_waitcnt vmcnt(3)
	v_mul_f32_e32 v34, s5, v46
	v_cvt_pk_fp8_f32 v67, v5, v13 op_sel:[0,0,1]
	s_waitcnt vmcnt(2)
	v_mul_f32_e32 v5, s5, v50
	v_med3_f32 v6, v19, s4, v22
	v_mul_f32_e32 v17, s5, v39
	v_mul_f32_e32 v19, s5, v43
	v_cvt_pk_fp8_f32 v2, v16, v7 op_sel:[0,0,1]
	v_cvt_pk_fp8_f32 v66, v4, v12 op_sel:[0,0,1]
	v_med3_f32 v4, v34, s4, v22
	v_med3_f32 v5, v5, s4, v22
	v_mul_f32_e32 v14, s5, v37
	v_med3_f32 v17, v17, s4, v22
	v_med3_f32 v19, v19, s4, v22
	v_cvt_pk_fp8_f32 v69, v4, v5 op_sel:[0,0,1]
	v_mov_b32_e32 v4, 0
	v_med3_f32 v14, v14, s4, v22
	v_cvt_pk_fp8_f32 v4, v17, v19
	v_cvt_pk_fp8_f32 v68, v6, v14 op_sel:[0,0,1]
	ds_write_b32 v26, v2 offset:16384
	ds_write_b32 v27, v66 offset:16640
	ds_write_b32 v30, v67 offset:16896
	ds_write_b32 v31, v68 offset:17152
	v_mul_f32_e32 v2, s5, v47
	v_mul_f32_e32 v5, s5, v51
	v_med3_f32 v2, v2, s4, v22
	v_med3_f32 v5, v5, s4, v22
	v_cvt_pk_fp8_f32 v4, v2, v5 op_sel:[0,0,1]
	v_mul_f32_e32 v2, s5, v40
	v_mul_f32_e32 v5, s5, v44
	v_med3_f32 v2, v2, s4, v22
	v_med3_f32 v5, v5, s4, v22
	v_mov_b32_e32 v7, 0
	v_cvt_pk_fp8_f32 v7, v2, v5
	v_mul_f32_e32 v6, s5, v48
	v_mul_f32_e32 v5, s5, v52
	v_med3_f32 v2, v6, s4, v22
	v_med3_f32 v5, v5, s4, v22
	v_cvt_pk_fp8_f32 v7, v2, v5 op_sel:[0,0,1]
	v_mul_f32_e32 v2, s5, v41
	v_mul_f32_e32 v5, s5, v45
	v_med3_f32 v2, v2, s4, v22
	v_med3_f32 v5, v5, s4, v22
	v_mov_b32_e32 v12, 0
	v_cvt_pk_fp8_f32 v12, v2, v5
	v_mul_f32_e32 v6, s5, v49
	v_mul_f32_e32 v5, s5, v53
	v_med3_f32 v2, v6, s4, v22
	v_med3_f32 v5, v5, s4, v22
	v_cvt_pk_fp8_f32 v12, v2, v5 op_sel:[0,0,1]
	ds_write_b32 v28, v69 offset:16384
	ds_write_b32 v29, v4 offset:16640
	ds_write_b32 v32, v7 offset:16896
	ds_write_b32 v33, v12 offset:17152
	s_waitcnt lgkmcnt(0)
	s_barrier
	ds_read_b128 v[4:7], v25 offset:16384
	ds_read_b128 v[12:15], v24 offset:16384
	v_mov_b64_e32 v[16:17], s[0:1]
	v_mad_u64_u32 v[16:17], s[0:1], s22, v23, v[16:17]
	v_lshl_add_u64 v[10:11], v[16:17], 0, v[10:11]
	s_waitcnt lgkmcnt(1)
	global_store_dwordx4 v[10:11], v[4:7], off
	s_mov_b64 s[0:1], -1
	s_nop 0
	v_lshl_add_u64 v[4:5], v[16:17], 0, v[8:9]
	s_waitcnt lgkmcnt(0)
	global_store_dwordx4 v[4:5], v[12:15], off
	s_barrier
